# stack8: stack5 + out-projection staging requests all 16 A chunks behind the small factor loads + QKV staging requests all modulation factors together
# baseline (speedup 1.0000x reference)
; #define REP(n) _Pragma("unroll 1") for (int rep_ = 0; rep_ < (n); ++rep_)
; DEVINL void phase2(const Params& P, unsigned char* smem, XPre& X, const bool have_pre) {
;     ...
;         if (!SKIPF(128)) REP(P2_RS) {
;             asm volatile("" ::: "memory");
;             const float* mb = mod + (m0 >> 13) * 6144;
;             f32x4 mul[4], sh[4];
; #pragma unroll
;             for (int j = 0; j < 4; ++j) { const int col = 4 * lane + 256 * j;
;                 mul[j] = *(const f32x4*)(P.g_pre_mix + col) * (*(const f32x4*)(mb + 1024 + col) + 1.f); sh[j] = *(const f32x4*)(mb + col); }
; #pragma unroll
.LBB0_177:
	v_readlane_b32 s4, v255, 17
	v_readlane_b32 s5, v255, 18
	s_lshl_b32 s0, s2, 6
	v_mov_b32_e32 v180, v1
	s_andn2_b64 vcc, exec, s[4:5]
	s_barrier
	s_cbranch_vccnz .LBB0_179
	s_lshr_b32 s1, s2, 7
	s_mul_i32 s4, s1, 0x1800
	s_ashr_i32 s5, s4, 31
	s_lshl_b64 s[4:5], s[4:5], 2
	v_readlane_b32 s1, v254, 45
	s_waitcnt vmcnt(7)
	v_lshlrev_b32_e32 v130, 2, v180
	s_add_u32 s4, s1, s4
	v_readlane_b32 s1, v254, 46
	v_ashrrev_i32_e32 v131, 31, v130
	s_addc_u32 s5, s1, s5
	s_waitcnt vmcnt(6)
	v_lshlrev_b64 v[134:135], 2, v[130:131]
	v_readlane_b32 s36, v254, 4
	v_readlane_b32 s44, v254, 12
	v_readlane_b32 s45, v254, 13
	v_lshl_add_u64 v[164:165], s[4:5], 0, v[134:135]
	v_readlane_b32 s6, v254, 47
	s_waitcnt vmcnt(3)
	v_lshl_add_u64 v[158:159], s[44:45], 0, v[134:135]
	v_add_co_u32_e32 v134, vcc, s56, v164
	v_readlane_b32 s7, v254, 48
	s_nop 0
	v_addc_co_u32_e32 v135, vcc, 0, v165, vcc
	v_lshlrev_b32_e32 v132, 3, v180
	global_load_dwordx4 v[134:137], v[134:135], off
	v_lshl_add_u64 v[162:163], v[130:131], 1, s[6:7]
	v_and_b32_e32 v168, 8, v132
	global_load_dwordx4 v[130:133], v[158:159], off
	s_mov_b64 s[4:5], 0x1000
	v_lshl_add_u64 v[160:161], v[164:165], 0, s[4:5]
	s_waitcnt vmcnt(31)
	v_mov_b32_e32 v169, v119
	s_add_i32 s4, s0, s3
	s_ashr_i32 s5, s4, 31
	s_lshl_b64 s[4:5], s[4:5], 11
	v_cvt_pk_bf16_f32 v170, v126, v127
	v_cvt_pk_bf16_f32 v171, v128, v129
	v_mov_b32_e32 v174, v122
	v_mov_b32_e32 v175, v126
	v_mov_b32_e32 v172, v125
	v_mov_b32_e32 v173, v129
	v_readlane_b32 s1, v254, 58
	s_waitcnt vmcnt(26)
	v_mov_b32_e32 v176, v99
	v_mov_b32_e32 v177, v103
	v_pk_mul_f32 v[176:177], v[176:177], v[176:177]
	v_cvt_pk_bf16_f32 v182, v110, v111
	v_cvt_pk_bf16_f32 v183, v112, v113
	v_mov_b32_e32 v186, v106
	v_mov_b32_e32 v187, v110
	v_mov_b32_e32 v184, v109
	v_mov_b32_e32 v185, v113
	s_mov_b32 s10, 0x3a800000
	s_mov_b32 s8, 0x800000
	v_readlane_b32 s37, v254, 5
	v_readlane_b32 s38, v254, 6
	v_readlane_b32 s39, v254, 7
	v_readlane_b32 s40, v254, 8
	v_readlane_b32 s41, v254, 9
	v_readlane_b32 s42, v254, 10
	v_readlane_b32 s43, v254, 11
	v_readlane_b32 s46, v254, 14
	v_readlane_b32 s47, v254, 15
	v_readlane_b32 s48, v254, 16
	v_readlane_b32 s49, v254, 17
	v_readlane_b32 s50, v254, 18
	v_readlane_b32 s51, v254, 19
	v_readlane_b32 s36, v254, 24
	v_readlane_b32 s42, v254, 30
	v_readlane_b32 s37, v254, 25
	v_readlane_b32 s38, v254, 26
	v_readlane_b32 s39, v254, 27
	v_readlane_b32 s40, v254, 28
	v_readlane_b32 s41, v254, 29
	v_readlane_b32 s46, v254, 34
	v_readlane_b32 s47, v254, 35
	v_readlane_b32 s48, v254, 36
	v_readlane_b32 s49, v254, 37
	v_readlane_b32 s50, v254, 38
	v_readlane_b32 s51, v254, 39
	s_mov_b32 s42, 0x9b00000
	v_readlane_b32 s43, v254, 31
	v_readlane_b32 s44, v254, 32
	v_readlane_b32 s45, v254, 33
	global_load_dwordx4 v[212:215], v[158:159], off offset:1024
	global_load_dwordx4 v[216:219], v[160:161], off offset:1024
	global_load_dwordx4 v[224:227], v[158:159], off offset:2048
	global_load_dwordx4 v[228:231], v[160:161], off offset:2048
	global_load_dwordx4 v[232:235], v[158:159], off offset:3072
	global_load_dwordx4 v[236:239], v[160:161], off offset:3072
	s_waitcnt vmcnt(7)
	v_pk_add_f32 v[136:137], v[136:137], 1.0 op_sel_hi:[1,0]
	v_pk_add_f32 v[134:135], v[134:135], 1.0 op_sel_hi:[1,0]
	s_waitcnt vmcnt(6)
	v_pk_mul_f32 v[146:147], v[132:133], v[136:137]
	v_pk_mul_f32 v[148:149], v[130:131], v[134:135]
	global_load_dwordx4 v[130:133], v[164:165], off
	global_load_dwordx4 v[134:137], v[164:165], off offset:1024
	global_load_dwordx4 v[138:141], v[164:165], off offset:2048
	global_load_dwordx4 v[142:145], v[164:165], off offset:3072
	s_waitcnt vmcnt(8)
	v_pk_add_f32 v[218:219], v[218:219], 1.0 op_sel_hi:[1,0]
	v_pk_add_f32 v[216:217], v[216:217], 1.0 op_sel_hi:[1,0]
	v_pk_mul_f32 v[150:151], v[214:215], v[218:219]
	v_pk_mul_f32 v[152:153], v[212:213], v[216:217]
	s_waitcnt vmcnt(6)
	v_pk_add_f32 v[230:231], v[230:231], 1.0 op_sel_hi:[1,0]
	v_pk_add_f32 v[228:229], v[228:229], 1.0 op_sel_hi:[1,0]
	v_pk_mul_f32 v[154:155], v[226:227], v[230:231]
	v_pk_mul_f32 v[156:157], v[224:225], v[228:229]
	s_waitcnt vmcnt(4)
	v_pk_add_f32 v[238:239], v[238:239], 1.0 op_sel_hi:[1,0]
	v_pk_add_f32 v[236:237], v[236:237], 1.0 op_sel_hi:[1,0]
	v_pk_mul_f32 v[158:159], v[234:235], v[238:239]
	v_pk_mul_f32 v[160:161], v[232:233], v[236:237]
	s_waitcnt vmcnt(1)
; DEVINL unsigned pk2(float lo, float hi) { const f32x2 v = {lo, hi}; return __builtin_bit_cast(unsigned, __builtin_convertvector(v, bf16v2)); }
; DEVINL void phase2(const Params& P, unsigned char* smem, XPre& X, const bool have_pre) {
;     ...
;             for (int rr = 0; rr < 8; ++rr) {
;                 const int row = 8 * wv + rr;
;                 f32x4 v[4]; float ss = 0.f;
; #pragma unroll
;                 for (int j = 0; j < 4; ++j) { v[j] = X.v[rr][j]; ss += v[j].x * v[j].x + v[j].y * v[j].y + v[j].z * v[j].z + v[j].w * v[j].w; }
; #pragma unroll
;                 for (int j = 0; j < 4; ++j) { u32x2 o; o.x = pk2(v[j].x, v[j].y); o.y = pk2(v[j].z, v[j].w); *(u32x2*)(XB + (size_t)(m0 + row) * DM + 4 * lane + 256 * j) = o; }
;                 ss = wave_sum(ss);
;                 const float rstd = rsqrtf(ss * (1.f / DM) + EPS);
; #pragma unroll
;                 for (int j = 0; j < 4; ++j) {
;                     const f32x4 h = v[j] * rstd * mul[j] + sh[j];
;                     u32x2 o; o.x = pk2(h.x, h.y); o.y = pk2(h.z, h.w);
;                     const int c = (lane >> 1) + 32 * j;
;                     *(u32x2*)(smem + row * 2048 + ((c ^ (row & 15)) << 4) + (lane & 1) * 8) = o;
;                 }
	v_add_u32_e32 v167, 0, v168
	v_mov_b32_e32 v168, v115
	v_mov_b32_e32 v164, v114
	v_mov_b32_e32 v165, v118
	v_pk_mul_f32 v[168:169], v[168:169], v[168:169]
	v_lshrrev_b32_e32 v166, 1, v180
	v_pk_fma_f32 v[164:165], v[164:165], v[164:165], v[168:169]
	v_mov_b32_e32 v168, v116
	v_mov_b32_e32 v169, v120
	v_pk_fma_f32 v[164:165], v[168:169], v[168:169], v[164:165]
	v_mov_b32_e32 v168, v117
	v_mov_b32_e32 v169, v121
	v_pk_fma_f32 v[164:165], v[168:169], v[168:169], v[164:165]
	v_lshl_add_u64 v[168:169], v[162:163], 0, s[4:5]
	global_store_dwordx2 v[168:169], v[170:171], off
	v_cvt_pk_bf16_f32 v170, v122, v123
	v_cvt_pk_bf16_f32 v171, v124, v125
	global_store_dwordx2 v[168:169], v[170:171], off offset:512
	v_cvt_pk_bf16_f32 v170, v118, v119
	v_cvt_pk_bf16_f32 v171, v120, v121
	global_store_dwordx2 v[168:169], v[170:171], off offset:1024
	v_cvt_pk_bf16_f32 v170, v114, v115
	v_cvt_pk_bf16_f32 v171, v116, v117
	global_store_dwordx2 v[168:169], v[170:171], off offset:1536
	v_mov_b32_e32 v168, v123
	v_mov_b32_e32 v169, v127
	v_pk_mul_f32 v[168:169], v[168:169], v[168:169]
	v_mov_b32_e32 v170, v124
	v_mov_b32_e32 v171, v128
	v_pk_fma_f32 v[168:169], v[174:175], v[174:175], v[168:169]
	v_mov_b32_e32 v174, v98
	v_pk_fma_f32 v[168:169], v[170:171], v[170:171], v[168:169]
	v_add_u32_e32 v170, 32, v166
	v_pk_fma_f32 v[168:169], v[172:173], v[172:173], v[168:169]
	v_mov_b32_e32 v175, v102
	v_pk_add_f32 v[168:169], v[168:169], v[168:169] op_sel:[0,1] op_sel_hi:[1,0]
	v_pk_fma_f32 v[174:175], v[174:175], v[174:175], v[176:177]
	v_pk_add_f32 v[168:169], v[164:165], v[168:169] op_sel:[1,0] op_sel_hi:[0,1]
	v_pk_add_f32 v[164:165], v[164:165], v[168:169]
	v_add_u32_e32 v169, 64, v166
	v_mov_b32_e32 v165, v164
	s_nop 1
	v_permlane16_swap_b32_e32 v164, v165
	v_add_f32_e32 v165, v164, v165
	v_add_u32_e32 v164, s1, v167
	v_readlane_b32 s1, v254, 59
	v_mov_b32_e32 v176, v100
	v_mov_b32_e32 v177, v104
	v_xor_b32_e32 v168, s1, v166
	v_lshl_add_u32 v171, v168, 4, v164
	v_xor_b32_e32 v168, s1, v170
	v_lshl_add_u32 v178, v168, 4, v164
	v_xor_b32_e32 v168, s1, v169
	v_lshl_add_u32 v181, v168, 4, v164
	v_add_u32_e32 v168, 0x60, v166
	v_xor_b32_e32 v172, s1, v168
	v_readlane_b32 s1, v254, 61
	s_add_i32 s4, s0, s1
	s_ashr_i32 s5, s4, 31
	v_pk_fma_f32 v[174:175], v[176:177], v[176:177], v[174:175]
	v_mov_b32_e32 v176, v101
	v_mov_b32_e32 v177, v105
	s_lshl_b64 s[4:5], s[4:5], 11
	v_pk_fma_f32 v[174:175], v[176:177], v[176:177], v[174:175]
	v_lshl_add_u64 v[176:177], v[162:163], 0, s[4:5]
	global_store_dwordx2 v[176:177], v[182:183], off
	v_cvt_pk_bf16_f32 v182, v106, v107
	v_cvt_pk_bf16_f32 v183, v108, v109
	global_store_dwordx2 v[176:177], v[182:183], off offset:512
	v_cvt_pk_bf16_f32 v182, v102, v103
	v_cvt_pk_bf16_f32 v183, v104, v105
	global_store_dwordx2 v[176:177], v[182:183], off offset:1024
	v_cvt_pk_bf16_f32 v182, v98, v99
	v_cvt_pk_bf16_f32 v183, v100, v101
	global_store_dwordx2 v[176:177], v[182:183], off offset:1536
	v_mov_b32_e32 v176, v107
	v_mov_b32_e32 v177, v111
	v_pk_mul_f32 v[176:177], v[176:177], v[176:177]
	v_mov_b32_e32 v182, v108
	v_mov_b32_e32 v183, v112
	v_pk_fma_f32 v[176:177], v[186:187], v[186:187], v[176:177]
	v_lshl_add_u32 v188, v172, 4, v164
	v_pk_fma_f32 v[176:177], v[182:183], v[182:183], v[176:177]
	v_mov_b32_e32 v173, v165
	v_pk_fma_f32 v[176:177], v[184:185], v[184:185], v[176:177]
	s_nop 0
	v_permlane32_swap_b32_e32 v165, v173
	v_pk_add_f32 v[176:177], v[176:177], v[176:177] op_sel:[0,1] op_sel_hi:[1,0]
	s_mov_b32 s4, 0x358637bd
	v_pk_add_f32 v[176:177], v[174:175], v[176:177] op_sel:[1,0] op_sel_hi:[0,1]
	v_pk_add_f32 v[174:175], v[174:175], v[176:177]
	v_readlane_b32 s1, v254, 60
	v_mov_b32_e32 v164, v174
	s_nop 1
	v_permlane16_swap_b32_e32 v174, v164
	v_add_f32_e32 v164, v174, v164
	v_mov_b32_e32 v172, v164
	s_nop 1
	v_permlane32_swap_b32_e32 v164, v172
	v_pk_add_f32 v[164:165], v[164:165], v[172:173]
	s_nop 1
	v_mov_b32_dpp v173, v165 quad_perm:[1,0,3,2] row_mask:0xf bank_mask:0xf bound_ctrl:1
	v_mov_b32_dpp v172, v164 quad_perm:[1,0,3,2] row_mask:0xf bank_mask:0xf bound_ctrl:1
	v_pk_add_f32 v[164:165], v[164:165], v[172:173]
	s_nop 1
	v_mov_b32_dpp v173, v165 quad_perm:[2,3,0,1] row_mask:0xf bank_mask:0xf bound_ctrl:1
	v_mov_b32_dpp v172, v164 quad_perm:[2,3,0,1] row_mask:0xf bank_mask:0xf bound_ctrl:1
	v_pk_add_f32 v[164:165], v[164:165], v[172:173]
	s_nop 1
	v_mov_b32_dpp v173, v165 row_half_mirror row_mask:0xf bank_mask:0xf bound_ctrl:1
	v_mov_b32_dpp v172, v164 row_half_mirror row_mask:0xf bank_mask:0xf bound_ctrl:1
	v_pk_add_f32 v[164:165], v[164:165], v[172:173]
	s_nop 1
	v_mov_b32_dpp v173, v165 row_mirror row_mask:0xf bank_mask:0xf bound_ctrl:1
	v_mov_b32_dpp v172, v164 row_mirror row_mask:0xf bank_mask:0xf bound_ctrl:1
	v_pk_add_f32 v[172:173], v[164:165], v[172:173]
	v_mov_b64_e32 v[164:165], s[4:5]
	v_pk_fma_f32 v[172:173], v[172:173], s[10:11], v[164:165] op_sel_hi:[1,0,0]
	s_nop 0
	v_mul_f32_e32 v174, 0x4b800000, v173
	v_cmp_gt_f32_e64 s[6:7], s8, v173
	v_cmp_gt_f32_e32 vcc, s8, v172
	s_nop 0
	v_cndmask_b32_e64 v173, v173, v174, s[6:7]
	v_rsq_f32_e32 v173, v173
	s_nop 0
	v_mul_f32_e32 v174, 0x45800000, v173
	v_cndmask_b32_e64 v174, v173, v174, s[6:7]
	v_pk_mul_f32 v[126:127], v[126:127], v[174:175] op_sel_hi:[1,0]
	v_pk_mul_f32 v[128:129], v[128:129], v[174:175] op_sel_hi:[1,0]
	v_pk_mul_f32 v[122:123], v[122:123], v[174:175] op_sel_hi:[1,0]
	v_pk_mul_f32 v[124:125], v[124:125], v[174:175] op_sel_hi:[1,0]
	v_pk_mul_f32 v[118:119], v[118:119], v[174:175] op_sel_hi:[1,0]
	v_pk_mul_f32 v[120:121], v[120:121], v[174:175] op_sel_hi:[1,0]
	v_pk_mul_f32 v[114:115], v[114:115], v[174:175] op_sel_hi:[1,0]
	v_pk_mul_f32 v[116:117], v[116:117], v[174:175] op_sel_hi:[1,0]
	v_pk_fma_f32 v[128:129], v[146:147], v[128:129], v[132:133]
	v_pk_fma_f32 v[126:127], v[148:149], v[126:127], v[130:131]
	v_pk_fma_f32 v[124:125], v[150:151], v[124:125], v[136:137]
	v_pk_fma_f32 v[122:123], v[152:153], v[122:123], v[134:135]
	v_pk_fma_f32 v[120:121], v[154:155], v[120:121], v[140:141]
	v_pk_fma_f32 v[118:119], v[156:157], v[118:119], v[138:139]
	s_waitcnt vmcnt(8)
; DEVINL unsigned pk2(float lo, float hi) { const f32x2 v = {lo, hi}; return __builtin_bit_cast(unsigned, __builtin_convertvector(v, bf16v2)); }
; DEVINL void phase2(const Params& P, unsigned char* smem, XPre& X, const bool have_pre) {
;     ...
;             for (int rr = 0; rr < 8; ++rr) {
;                 const int row = 8 * wv + rr;
;                 f32x4 v[4]; float ss = 0.f;
; #pragma unroll
;                 for (int j = 0; j < 4; ++j) { v[j] = X.v[rr][j]; ss += v[j].x * v[j].x + v[j].y * v[j].y + v[j].z * v[j].z + v[j].w * v[j].w; }
; #pragma unroll
;                 for (int j = 0; j < 4; ++j) { u32x2 o; o.x = pk2(v[j].x, v[j].y); o.y = pk2(v[j].z, v[j].w); *(u32x2*)(XB + (size_t)(m0 + row) * DM + 4 * lane + 256 * j) = o; }
;                 ss = wave_sum(ss);
;                 const float rstd = rsqrtf(ss * (1.f / DM) + EPS);
; #pragma unroll
;                 for (int j = 0; j < 4; ++j) {
;                     const f32x4 h = v[j] * rstd * mul[j] + sh[j];
;                     u32x2 o; o.x = pk2(h.x, h.y); o.y = pk2(h.z, h.w);
;                     const int c = (lane >> 1) + 32 * j;
;                     *(u32x2*)(smem + row * 2048 + ((c ^ (row & 15)) << 4) + (lane & 1) * 8) = o;
;                 }
	v_pk_fma_f32 v[116:117], v[158:159], v[116:117], v[144:145]
	v_pk_fma_f32 v[114:115], v[160:161], v[114:115], v[142:143]
	v_cvt_pk_bf16_f32 v126, v126, v127
	v_cvt_pk_bf16_f32 v127, v128, v129
	v_cvt_pk_bf16_f32 v122, v122, v123
	v_cvt_pk_bf16_f32 v123, v124, v125
	v_cvt_pk_bf16_f32 v118, v118, v119
	v_cvt_pk_bf16_f32 v119, v120, v121
	v_cvt_pk_bf16_f32 v114, v114, v115
	v_cvt_pk_bf16_f32 v115, v116, v117
	ds_write_b64 v171, v[126:127]
	ds_write_b64 v178, v[122:123]
	ds_write_b64 v181, v[118:119]
	ds_write_b64 v188, v[114:115]
	v_mul_f32_e32 v114, 0x4b800000, v172
	v_cndmask_b32_e32 v114, v172, v114, vcc
	v_rsq_f32_e32 v114, v114
	s_nop 0
	v_mul_f32_e32 v115, 0x45800000, v114
	v_cndmask_b32_e32 v114, v114, v115, vcc
	v_add_u32_e32 v115, s1, v167
	v_pk_mul_f32 v[110:111], v[110:111], v[114:115] op_sel_hi:[1,0]
	v_pk_mul_f32 v[112:113], v[112:113], v[114:115] op_sel_hi:[1,0]
	v_pk_mul_f32 v[106:107], v[106:107], v[114:115] op_sel_hi:[1,0]
	v_pk_mul_f32 v[108:109], v[108:109], v[114:115] op_sel_hi:[1,0]
	v_pk_mul_f32 v[102:103], v[102:103], v[114:115] op_sel_hi:[1,0]
	v_pk_mul_f32 v[104:105], v[104:105], v[114:115] op_sel_hi:[1,0]
	v_pk_mul_f32 v[98:99], v[98:99], v[114:115] op_sel_hi:[1,0]
	v_pk_mul_f32 v[100:101], v[100:101], v[114:115] op_sel_hi:[1,0]
	v_pk_fma_f32 v[112:113], v[146:147], v[112:113], v[132:133]
	v_pk_fma_f32 v[110:111], v[148:149], v[110:111], v[130:131]
	v_readlane_b32 s1, v254, 62
	v_pk_fma_f32 v[108:109], v[150:151], v[108:109], v[136:137]
	v_pk_fma_f32 v[106:107], v[152:153], v[106:107], v[134:135]
	v_pk_fma_f32 v[104:105], v[154:155], v[104:105], v[140:141]
	v_pk_fma_f32 v[102:103], v[156:157], v[102:103], v[138:139]
	v_pk_fma_f32 v[100:101], v[158:159], v[100:101], v[144:145]
	v_pk_fma_f32 v[98:99], v[160:161], v[98:99], v[142:143]
	v_cvt_pk_bf16_f32 v110, v110, v111
	v_cvt_pk_bf16_f32 v111, v112, v113
	v_xor_b32_e32 v112, s1, v166
	v_cvt_pk_bf16_f32 v106, v106, v107
	v_cvt_pk_bf16_f32 v107, v108, v109
	v_xor_b32_e32 v108, s1, v170
	v_cvt_pk_bf16_f32 v102, v102, v103
	v_cvt_pk_bf16_f32 v103, v104, v105
	v_xor_b32_e32 v104, s1, v169
	v_cvt_pk_bf16_f32 v98, v98, v99
	v_cvt_pk_bf16_f32 v99, v100, v101
	v_xor_b32_e32 v100, s1, v168
	v_lshl_add_u32 v112, v112, 4, v115
	v_lshl_add_u32 v108, v108, 4, v115
	v_lshl_add_u32 v104, v104, 4, v115
	v_lshl_add_u32 v100, v100, 4, v115
	ds_write_b64 v112, v[110:111]
	ds_write_b64 v108, v[106:107]
	ds_write_b64 v104, v[102:103]
	ds_write_b64 v100, v[98:99]
	v_mov_b32_e32 v100, v83
	v_mov_b32_e32 v101, v87
	v_readlane_b32 s1, v255, 0
	v_mov_b32_e32 v98, v82
	v_mov_b32_e32 v99, v86
	v_pk_mul_f32 v[100:101], v[100:101], v[100:101]
	s_add_i32 s4, s0, s1
	v_pk_fma_f32 v[98:99], v[98:99], v[98:99], v[100:101]
	v_mov_b32_e32 v100, v84
	v_mov_b32_e32 v101, v88
	s_ashr_i32 s5, s4, 31
	v_pk_fma_f32 v[98:99], v[100:101], v[100:101], v[98:99]
	v_mov_b32_e32 v100, v85
	v_mov_b32_e32 v101, v89
	s_lshl_b64 s[4:5], s[4:5], 11
	v_pk_fma_f32 v[98:99], v[100:101], v[100:101], v[98:99]
	v_lshl_add_u64 v[100:101], v[162:163], 0, s[4:5]
	v_cvt_pk_bf16_f32 v102, v94, v95
	v_cvt_pk_bf16_f32 v103, v96, v97
	global_store_dwordx2 v[100:101], v[102:103], off
	v_cvt_pk_bf16_f32 v102, v90, v91
	v_cvt_pk_bf16_f32 v103, v92, v93
	global_store_dwordx2 v[100:101], v[102:103], off offset:512
	v_cvt_pk_bf16_f32 v102, v86, v87
	v_cvt_pk_bf16_f32 v103, v88, v89
	global_store_dwordx2 v[100:101], v[102:103], off offset:1024
	v_cvt_pk_bf16_f32 v102, v82, v83
	v_cvt_pk_bf16_f32 v103, v84, v85
	global_store_dwordx2 v[100:101], v[102:103], off offset:1536
	v_mov_b32_e32 v100, v91
	v_mov_b32_e32 v101, v95
	v_pk_mul_f32 v[100:101], v[100:101], v[100:101]
	v_mov_b32_e32 v106, v90
	v_mov_b32_e32 v107, v94
	v_mov_b32_e32 v102, v92
	v_mov_b32_e32 v103, v96
	v_pk_fma_f32 v[100:101], v[106:107], v[106:107], v[100:101]
	v_mov_b32_e32 v104, v93
	v_mov_b32_e32 v105, v97
	v_pk_fma_f32 v[100:101], v[102:103], v[102:103], v[100:101]
	v_readlane_b32 s1, v254, 63
	v_pk_fma_f32 v[100:101], v[104:105], v[104:105], v[100:101]
	v_mov_b32_e32 v104, v67
	v_pk_add_f32 v[100:101], v[100:101], v[100:101] op_sel:[0,1] op_sel_hi:[1,0]
	v_mov_b32_e32 v105, v71
	v_pk_add_f32 v[100:101], v[98:99], v[100:101] op_sel:[1,0] op_sel_hi:[0,1]
	v_pk_add_f32 v[98:99], v[98:99], v[100:101]
	v_mov_b32_e32 v102, v66
	v_mov_b32_e32 v99, v98
	s_nop 1
	v_permlane16_swap_b32_e32 v98, v99
	v_add_f32_e32 v99, v98, v99
	v_add_u32_e32 v98, s1, v167
	v_readlane_b32 s1, v255, 1
	v_mov_b32_e32 v103, v70
	v_pk_mul_f32 v[104:105], v[104:105], v[104:105]
	v_xor_b32_e32 v100, s1, v166
	v_lshl_add_u32 v112, v100, 4, v98
	v_xor_b32_e32 v100, s1, v170
	v_lshl_add_u32 v113, v100, 4, v98
	v_xor_b32_e32 v100, s1, v169
	v_lshl_add_u32 v114, v100, 4, v98
	v_xor_b32_e32 v100, s1, v168
	v_readlane_b32 s1, v255, 3
	s_add_i32 s4, s0, s1
	v_pk_fma_f32 v[102:103], v[102:103], v[102:103], v[104:105]
	v_mov_b32_e32 v104, v68
	v_mov_b32_e32 v105, v72
	s_ashr_i32 s5, s4, 31
	v_pk_fma_f32 v[102:103], v[104:105], v[104:105], v[102:103]
	v_mov_b32_e32 v104, v69
	v_mov_b32_e32 v105, v73
	s_lshl_b64 s[4:5], s[4:5], 11
	v_pk_fma_f32 v[102:103], v[104:105], v[104:105], v[102:103]
	v_lshl_add_u64 v[104:105], v[162:163], 0, s[4:5]
	v_cvt_pk_bf16_f32 v106, v78, v79
	v_cvt_pk_bf16_f32 v107, v80, v81
	global_store_dwordx2 v[104:105], v[106:107], off
	v_cvt_pk_bf16_f32 v106, v74, v75
	v_cvt_pk_bf16_f32 v107, v76, v77
	global_store_dwordx2 v[104:105], v[106:107], off offset:512
	v_cvt_pk_bf16_f32 v106, v70, v71
	v_cvt_pk_bf16_f32 v107, v72, v73
	global_store_dwordx2 v[104:105], v[106:107], off offset:1024
	v_cvt_pk_bf16_f32 v106, v66, v67
	v_cvt_pk_bf16_f32 v107, v68, v69
	global_store_dwordx2 v[104:105], v[106:107], off offset:1536
; DEVINL unsigned pk2(float lo, float hi) { const f32x2 v = {lo, hi}; return __builtin_bit_cast(unsigned, __builtin_convertvector(v, bf16v2)); }
; DEVINL void phase2(const Params& P, unsigned char* smem, XPre& X, const bool have_pre) {
;     ...
;             for (int rr = 0; rr < 8; ++rr) {
;                 const int row = 8 * wv + rr;
;                 f32x4 v[4]; float ss = 0.f;
; #pragma unroll
;                 for (int j = 0; j < 4; ++j) { v[j] = X.v[rr][j]; ss += v[j].x * v[j].x + v[j].y * v[j].y + v[j].z * v[j].z + v[j].w * v[j].w; }
; #pragma unroll
;                 for (int j = 0; j < 4; ++j) { u32x2 o; o.x = pk2(v[j].x, v[j].y); o.y = pk2(v[j].z, v[j].w); *(u32x2*)(XB + (size_t)(m0 + row) * DM + 4 * lane + 256 * j) = o; }
;                 ss = wave_sum(ss);
;                 const float rstd = rsqrtf(ss * (1.f / DM) + EPS);
; #pragma unroll
;                 for (int j = 0; j < 4; ++j) {
;                     const f32x4 h = v[j] * rstd * mul[j] + sh[j];
;                     u32x2 o; o.x = pk2(h.x, h.y); o.y = pk2(h.z, h.w);
;                     const int c = (lane >> 1) + 32 * j;
;                     *(u32x2*)(smem + row * 2048 + ((c ^ (row & 15)) << 4) + (lane & 1) * 8) = o;
;                 }
	v_mov_b32_e32 v104, v75
	v_mov_b32_e32 v105, v79
	v_pk_mul_f32 v[104:105], v[104:105], v[104:105]
	v_mov_b32_e32 v110, v74
	v_mov_b32_e32 v111, v78
	v_mov_b32_e32 v106, v76
	v_mov_b32_e32 v107, v80
	v_pk_fma_f32 v[104:105], v[110:111], v[110:111], v[104:105]
	v_mov_b32_e32 v108, v77
	v_mov_b32_e32 v109, v81
	v_pk_fma_f32 v[104:105], v[106:107], v[106:107], v[104:105]
	v_lshl_add_u32 v115, v100, 4, v98
	v_pk_fma_f32 v[104:105], v[108:109], v[108:109], v[104:105]
	v_mov_b32_e32 v101, v99
	v_pk_add_f32 v[104:105], v[104:105], v[104:105] op_sel:[0,1] op_sel_hi:[1,0]
	s_nop 0
	v_permlane32_swap_b32_e32 v99, v101
	v_pk_add_f32 v[104:105], v[102:103], v[104:105] op_sel:[1,0] op_sel_hi:[0,1]
	v_pk_add_f32 v[102:103], v[102:103], v[104:105]
	v_readlane_b32 s1, v255, 2
	v_mov_b32_e32 v98, v102
	s_nop 1
	v_permlane16_swap_b32_e32 v102, v98
	v_add_f32_e32 v98, v102, v98
	v_mov_b32_e32 v100, v98
	s_nop 1
	v_permlane32_swap_b32_e32 v98, v100
	v_pk_add_f32 v[98:99], v[98:99], v[100:101]
	s_nop 1
	v_mov_b32_dpp v101, v99 quad_perm:[1,0,3,2] row_mask:0xf bank_mask:0xf bound_ctrl:1
	v_mov_b32_dpp v100, v98 quad_perm:[1,0,3,2] row_mask:0xf bank_mask:0xf bound_ctrl:1
	v_pk_add_f32 v[98:99], v[98:99], v[100:101]
	s_nop 1
	v_mov_b32_dpp v101, v99 quad_perm:[2,3,0,1] row_mask:0xf bank_mask:0xf bound_ctrl:1
	v_mov_b32_dpp v100, v98 quad_perm:[2,3,0,1] row_mask:0xf bank_mask:0xf bound_ctrl:1
	v_pk_add_f32 v[98:99], v[98:99], v[100:101]
	s_nop 1
	v_mov_b32_dpp v101, v99 row_half_mirror row_mask:0xf bank_mask:0xf bound_ctrl:1
	v_mov_b32_dpp v100, v98 row_half_mirror row_mask:0xf bank_mask:0xf bound_ctrl:1
	v_pk_add_f32 v[98:99], v[98:99], v[100:101]
	s_nop 1
	v_mov_b32_dpp v101, v99 row_mirror row_mask:0xf bank_mask:0xf bound_ctrl:1
	v_mov_b32_dpp v100, v98 row_mirror row_mask:0xf bank_mask:0xf bound_ctrl:1
	v_pk_add_f32 v[98:99], v[98:99], v[100:101]
	s_nop 0
	v_pk_fma_f32 v[98:99], v[98:99], s[10:11], v[164:165] op_sel_hi:[1,0,0]
	s_nop 0
	v_mul_f32_e32 v100, 0x4b800000, v99
	v_cmp_gt_f32_e64 s[6:7], s8, v99
	v_cmp_gt_f32_e32 vcc, s8, v98
	s_nop 0
	v_cndmask_b32_e64 v99, v99, v100, s[6:7]
	v_rsq_f32_e32 v99, v99
	s_nop 0
	v_mul_f32_e32 v100, 0x45800000, v99
	v_cndmask_b32_e64 v100, v99, v100, s[6:7]
	v_pk_mul_f32 v[94:95], v[94:95], v[100:101] op_sel_hi:[1,0]
	v_pk_mul_f32 v[96:97], v[96:97], v[100:101] op_sel_hi:[1,0]
	v_pk_mul_f32 v[90:91], v[90:91], v[100:101] op_sel_hi:[1,0]
	v_pk_mul_f32 v[92:93], v[92:93], v[100:101] op_sel_hi:[1,0]
	v_pk_mul_f32 v[86:87], v[86:87], v[100:101] op_sel_hi:[1,0]
	v_pk_mul_f32 v[88:89], v[88:89], v[100:101] op_sel_hi:[1,0]
	v_pk_mul_f32 v[82:83], v[82:83], v[100:101] op_sel_hi:[1,0]
	v_pk_mul_f32 v[84:85], v[84:85], v[100:101] op_sel_hi:[1,0]
	v_pk_fma_f32 v[96:97], v[146:147], v[96:97], v[132:133]
	v_pk_fma_f32 v[94:95], v[148:149], v[94:95], v[130:131]
	v_pk_fma_f32 v[92:93], v[150:151], v[92:93], v[136:137]
	v_pk_fma_f32 v[90:91], v[152:153], v[90:91], v[134:135]
	v_pk_fma_f32 v[88:89], v[154:155], v[88:89], v[140:141]
	v_pk_fma_f32 v[86:87], v[156:157], v[86:87], v[138:139]
	v_pk_fma_f32 v[84:85], v[158:159], v[84:85], v[144:145]
	v_pk_fma_f32 v[82:83], v[160:161], v[82:83], v[142:143]
	v_cvt_pk_bf16_f32 v94, v94, v95
	v_cvt_pk_bf16_f32 v95, v96, v97
	v_cvt_pk_bf16_f32 v90, v90, v91
	v_cvt_pk_bf16_f32 v91, v92, v93
	v_cvt_pk_bf16_f32 v86, v86, v87
	v_cvt_pk_bf16_f32 v87, v88, v89
	v_cvt_pk_bf16_f32 v82, v82, v83
	v_cvt_pk_bf16_f32 v83, v84, v85
	ds_write_b64 v112, v[94:95]
	ds_write_b64 v113, v[90:91]
	ds_write_b64 v114, v[86:87]
	ds_write_b64 v115, v[82:83]
	v_mul_f32_e32 v82, 0x4b800000, v98
	v_cndmask_b32_e32 v82, v98, v82, vcc
	v_rsq_f32_e32 v82, v82
	s_nop 0
	v_mul_f32_e32 v83, 0x45800000, v82
	v_cndmask_b32_e32 v82, v82, v83, vcc
	v_add_u32_e32 v83, s1, v167
	v_pk_mul_f32 v[78:79], v[78:79], v[82:83] op_sel_hi:[1,0]
	v_pk_mul_f32 v[80:81], v[80:81], v[82:83] op_sel_hi:[1,0]
	v_pk_mul_f32 v[74:75], v[74:75], v[82:83] op_sel_hi:[1,0]
	v_pk_mul_f32 v[76:77], v[76:77], v[82:83] op_sel_hi:[1,0]
	v_pk_mul_f32 v[70:71], v[70:71], v[82:83] op_sel_hi:[1,0]
	v_pk_mul_f32 v[72:73], v[72:73], v[82:83] op_sel_hi:[1,0]
	v_pk_mul_f32 v[66:67], v[66:67], v[82:83] op_sel_hi:[1,0]
	v_pk_mul_f32 v[68:69], v[68:69], v[82:83] op_sel_hi:[1,0]
	v_pk_fma_f32 v[80:81], v[146:147], v[80:81], v[132:133]
	v_pk_fma_f32 v[78:79], v[148:149], v[78:79], v[130:131]
	v_readlane_b32 s1, v255, 4
	v_pk_fma_f32 v[76:77], v[150:151], v[76:77], v[136:137]
	v_pk_fma_f32 v[74:75], v[152:153], v[74:75], v[134:135]
	v_pk_fma_f32 v[72:73], v[154:155], v[72:73], v[140:141]
	v_pk_fma_f32 v[70:71], v[156:157], v[70:71], v[138:139]
	v_pk_fma_f32 v[68:69], v[158:159], v[68:69], v[144:145]
	v_pk_fma_f32 v[66:67], v[160:161], v[66:67], v[142:143]
	v_cvt_pk_bf16_f32 v78, v78, v79
	v_cvt_pk_bf16_f32 v79, v80, v81
	v_xor_b32_e32 v80, s1, v166
	v_cvt_pk_bf16_f32 v74, v74, v75
	v_cvt_pk_bf16_f32 v75, v76, v77
	v_xor_b32_e32 v76, s1, v170
	v_cvt_pk_bf16_f32 v70, v70, v71
	v_cvt_pk_bf16_f32 v71, v72, v73
	v_xor_b32_e32 v72, s1, v169
	v_cvt_pk_bf16_f32 v66, v66, v67
	v_cvt_pk_bf16_f32 v67, v68, v69
	v_xor_b32_e32 v68, s1, v168
	v_lshl_add_u32 v80, v80, 4, v83
	v_lshl_add_u32 v76, v76, 4, v83
	v_lshl_add_u32 v72, v72, 4, v83
	v_lshl_add_u32 v68, v68, 4, v83
	ds_write_b64 v80, v[78:79]
	ds_write_b64 v76, v[74:75]
	ds_write_b64 v72, v[70:71]
	ds_write_b64 v68, v[66:67]
	v_mov_b32_e32 v68, v51
	v_mov_b32_e32 v69, v55
	v_readlane_b32 s1, v255, 6
	v_mov_b32_e32 v66, v50
	v_mov_b32_e32 v67, v54
	v_pk_mul_f32 v[68:69], v[68:69], v[68:69]
	s_add_i32 s4, s0, s1
	v_pk_fma_f32 v[66:67], v[66:67], v[66:67], v[68:69]
	v_mov_b32_e32 v68, v52
	v_mov_b32_e32 v69, v56
	s_ashr_i32 s5, s4, 31
; DEVINL unsigned pk2(float lo, float hi) { const f32x2 v = {lo, hi}; return __builtin_bit_cast(unsigned, __builtin_convertvector(v, bf16v2)); }
; DEVINL void phase2(const Params& P, unsigned char* smem, XPre& X, const bool have_pre) {
;     ...
;             for (int rr = 0; rr < 8; ++rr) {
;                 const int row = 8 * wv + rr;
;                 f32x4 v[4]; float ss = 0.f;
; #pragma unroll
;                 for (int j = 0; j < 4; ++j) { v[j] = X.v[rr][j]; ss += v[j].x * v[j].x + v[j].y * v[j].y + v[j].z * v[j].z + v[j].w * v[j].w; }
; #pragma unroll
;                 for (int j = 0; j < 4; ++j) { u32x2 o; o.x = pk2(v[j].x, v[j].y); o.y = pk2(v[j].z, v[j].w); *(u32x2*)(XB + (size_t)(m0 + row) * DM + 4 * lane + 256 * j) = o; }
;                 ss = wave_sum(ss);
;                 const float rstd = rsqrtf(ss * (1.f / DM) + EPS);
; #pragma unroll
;                 for (int j = 0; j < 4; ++j) {
;                     const f32x4 h = v[j] * rstd * mul[j] + sh[j];
;                     u32x2 o; o.x = pk2(h.x, h.y); o.y = pk2(h.z, h.w);
;                     const int c = (lane >> 1) + 32 * j;
;                     *(u32x2*)(smem + row * 2048 + ((c ^ (row & 15)) << 4) + (lane & 1) * 8) = o;
;                 }
	v_pk_fma_f32 v[66:67], v[68:69], v[68:69], v[66:67]
	v_mov_b32_e32 v68, v53
	v_mov_b32_e32 v69, v57
	s_lshl_b64 s[4:5], s[4:5], 11
	v_pk_fma_f32 v[66:67], v[68:69], v[68:69], v[66:67]
	v_lshl_add_u64 v[68:69], v[162:163], 0, s[4:5]
	v_cvt_pk_bf16_f32 v70, v62, v63
	v_cvt_pk_bf16_f32 v71, v64, v65
	global_store_dwordx2 v[68:69], v[70:71], off
	v_cvt_pk_bf16_f32 v70, v58, v59
	v_cvt_pk_bf16_f32 v71, v60, v61
	global_store_dwordx2 v[68:69], v[70:71], off offset:512
	v_cvt_pk_bf16_f32 v70, v54, v55
	v_cvt_pk_bf16_f32 v71, v56, v57
	global_store_dwordx2 v[68:69], v[70:71], off offset:1024
	v_cvt_pk_bf16_f32 v70, v50, v51
	v_cvt_pk_bf16_f32 v71, v52, v53
	global_store_dwordx2 v[68:69], v[70:71], off offset:1536
	v_mov_b32_e32 v68, v59
	v_mov_b32_e32 v69, v63
	v_pk_mul_f32 v[68:69], v[68:69], v[68:69]
	v_mov_b32_e32 v74, v58
	v_mov_b32_e32 v75, v62
	v_mov_b32_e32 v70, v60
	v_mov_b32_e32 v71, v64
	v_pk_fma_f32 v[68:69], v[74:75], v[74:75], v[68:69]
	v_mov_b32_e32 v72, v61
	v_mov_b32_e32 v73, v65
	v_pk_fma_f32 v[68:69], v[70:71], v[70:71], v[68:69]
	v_readlane_b32 s1, v255, 5
	v_pk_fma_f32 v[68:69], v[72:73], v[72:73], v[68:69]
	v_mov_b32_e32 v72, v35
	v_pk_add_f32 v[68:69], v[68:69], v[68:69] op_sel:[0,1] op_sel_hi:[1,0]
	v_mov_b32_e32 v73, v39
	v_pk_add_f32 v[68:69], v[66:67], v[68:69] op_sel:[1,0] op_sel_hi:[0,1]
	v_pk_add_f32 v[66:67], v[66:67], v[68:69]
	v_mov_b32_e32 v70, v34
	v_mov_b32_e32 v67, v66
	s_nop 1
	v_permlane16_swap_b32_e32 v66, v67
	v_add_f32_e32 v67, v66, v67
	v_add_u32_e32 v66, s1, v167
	v_readlane_b32 s1, v255, 7
	v_mov_b32_e32 v71, v38
	v_pk_mul_f32 v[72:73], v[72:73], v[72:73]
	v_xor_b32_e32 v68, s1, v166
	v_lshl_add_u32 v80, v68, 4, v66
	v_xor_b32_e32 v68, s1, v170
	v_lshl_add_u32 v81, v68, 4, v66
	v_xor_b32_e32 v68, s1, v169
	v_lshl_add_u32 v82, v68, 4, v66
	v_xor_b32_e32 v68, s1, v168
	v_readlane_b32 s1, v255, 9
	s_add_i32 s4, s0, s1
	v_pk_fma_f32 v[70:71], v[70:71], v[70:71], v[72:73]
	v_mov_b32_e32 v72, v36
	v_mov_b32_e32 v73, v40
	s_ashr_i32 s5, s4, 31
	v_pk_fma_f32 v[70:71], v[72:73], v[72:73], v[70:71]
	v_mov_b32_e32 v72, v37
	v_mov_b32_e32 v73, v41
	s_lshl_b64 s[4:5], s[4:5], 11
	v_pk_fma_f32 v[70:71], v[72:73], v[72:73], v[70:71]
	v_lshl_add_u64 v[72:73], v[162:163], 0, s[4:5]
	v_cvt_pk_bf16_f32 v74, v46, v47
	v_cvt_pk_bf16_f32 v75, v48, v49
	global_store_dwordx2 v[72:73], v[74:75], off
	v_cvt_pk_bf16_f32 v74, v42, v43
	v_cvt_pk_bf16_f32 v75, v44, v45
	global_store_dwordx2 v[72:73], v[74:75], off offset:512
	v_cvt_pk_bf16_f32 v74, v38, v39
	v_cvt_pk_bf16_f32 v75, v40, v41
	global_store_dwordx2 v[72:73], v[74:75], off offset:1024
	v_cvt_pk_bf16_f32 v74, v34, v35
	v_cvt_pk_bf16_f32 v75, v36, v37
	global_store_dwordx2 v[72:73], v[74:75], off offset:1536
	v_mov_b32_e32 v72, v43
	v_mov_b32_e32 v73, v47
	v_pk_mul_f32 v[72:73], v[72:73], v[72:73]
	v_mov_b32_e32 v78, v42
	v_mov_b32_e32 v79, v46
	v_mov_b32_e32 v74, v44
	v_mov_b32_e32 v75, v48
	v_pk_fma_f32 v[72:73], v[78:79], v[78:79], v[72:73]
	v_mov_b32_e32 v76, v45
	v_mov_b32_e32 v77, v49
	v_pk_fma_f32 v[72:73], v[74:75], v[74:75], v[72:73]
	v_lshl_add_u32 v83, v68, 4, v66
	v_pk_fma_f32 v[72:73], v[76:77], v[76:77], v[72:73]
	v_mov_b32_e32 v69, v67
	v_pk_add_f32 v[72:73], v[72:73], v[72:73] op_sel:[0,1] op_sel_hi:[1,0]
	s_nop 0
	v_permlane32_swap_b32_e32 v67, v69
	v_pk_add_f32 v[72:73], v[70:71], v[72:73] op_sel:[1,0] op_sel_hi:[0,1]
	v_pk_add_f32 v[70:71], v[70:71], v[72:73]
	v_readlane_b32 s1, v255, 8
	v_mov_b32_e32 v66, v70
	s_nop 1
	v_permlane16_swap_b32_e32 v70, v66
	v_add_f32_e32 v66, v70, v66
	v_mov_b32_e32 v68, v66
	s_nop 1
	v_permlane32_swap_b32_e32 v66, v68
	v_pk_add_f32 v[66:67], v[66:67], v[68:69]
	s_nop 1
	v_mov_b32_dpp v69, v67 quad_perm:[1,0,3,2] row_mask:0xf bank_mask:0xf bound_ctrl:1
	v_mov_b32_dpp v68, v66 quad_perm:[1,0,3,2] row_mask:0xf bank_mask:0xf bound_ctrl:1
	v_pk_add_f32 v[66:67], v[66:67], v[68:69]
	s_nop 1
	v_mov_b32_dpp v69, v67 quad_perm:[2,3,0,1] row_mask:0xf bank_mask:0xf bound_ctrl:1
	v_mov_b32_dpp v68, v66 quad_perm:[2,3,0,1] row_mask:0xf bank_mask:0xf bound_ctrl:1
	v_pk_add_f32 v[66:67], v[66:67], v[68:69]
	s_nop 1
	v_mov_b32_dpp v69, v67 row_half_mirror row_mask:0xf bank_mask:0xf bound_ctrl:1
	v_mov_b32_dpp v68, v66 row_half_mirror row_mask:0xf bank_mask:0xf bound_ctrl:1
	v_pk_add_f32 v[66:67], v[66:67], v[68:69]
	s_nop 1
	v_mov_b32_dpp v69, v67 row_mirror row_mask:0xf bank_mask:0xf bound_ctrl:1
	v_mov_b32_dpp v68, v66 row_mirror row_mask:0xf bank_mask:0xf bound_ctrl:1
	v_pk_add_f32 v[66:67], v[66:67], v[68:69]
	s_nop 0
	v_pk_fma_f32 v[66:67], v[66:67], s[10:11], v[164:165] op_sel_hi:[1,0,0]
	s_nop 0
	v_mul_f32_e32 v68, 0x4b800000, v67
	v_cmp_gt_f32_e64 s[6:7], s8, v67
	v_cmp_gt_f32_e32 vcc, s8, v66
	s_nop 0
	v_cndmask_b32_e64 v67, v67, v68, s[6:7]
	v_rsq_f32_e32 v67, v67
	s_nop 0
	v_mul_f32_e32 v68, 0x45800000, v67
	v_cndmask_b32_e64 v68, v67, v68, s[6:7]
	v_pk_mul_f32 v[62:63], v[62:63], v[68:69] op_sel_hi:[1,0]
	v_pk_mul_f32 v[64:65], v[64:65], v[68:69] op_sel_hi:[1,0]
	v_pk_mul_f32 v[58:59], v[58:59], v[68:69] op_sel_hi:[1,0]
	v_pk_mul_f32 v[60:61], v[60:61], v[68:69] op_sel_hi:[1,0]
	v_pk_mul_f32 v[54:55], v[54:55], v[68:69] op_sel_hi:[1,0]
	v_pk_mul_f32 v[56:57], v[56:57], v[68:69] op_sel_hi:[1,0]
	v_pk_mul_f32 v[50:51], v[50:51], v[68:69] op_sel_hi:[1,0]
	v_pk_mul_f32 v[52:53], v[52:53], v[68:69] op_sel_hi:[1,0]
	v_pk_fma_f32 v[64:65], v[146:147], v[64:65], v[132:133]
	v_pk_fma_f32 v[62:63], v[148:149], v[62:63], v[130:131]
	v_pk_fma_f32 v[60:61], v[150:151], v[60:61], v[136:137]
	v_pk_fma_f32 v[58:59], v[152:153], v[58:59], v[134:135]
	v_pk_fma_f32 v[56:57], v[154:155], v[56:57], v[140:141]
	v_pk_fma_f32 v[54:55], v[156:157], v[54:55], v[138:139]
; DEVINL unsigned pk2(float lo, float hi) { const f32x2 v = {lo, hi}; return __builtin_bit_cast(unsigned, __builtin_convertvector(v, bf16v2)); }
; DEVINL void phase2(const Params& P, unsigned char* smem, XPre& X, const bool have_pre) {
;     ...
;             for (int rr = 0; rr < 8; ++rr) {
;                 const int row = 8 * wv + rr;
;                 f32x4 v[4]; float ss = 0.f;
; #pragma unroll
;                 for (int j = 0; j < 4; ++j) { v[j] = X.v[rr][j]; ss += v[j].x * v[j].x + v[j].y * v[j].y + v[j].z * v[j].z + v[j].w * v[j].w; }
; #pragma unroll
;                 for (int j = 0; j < 4; ++j) { u32x2 o; o.x = pk2(v[j].x, v[j].y); o.y = pk2(v[j].z, v[j].w); *(u32x2*)(XB + (size_t)(m0 + row) * DM + 4 * lane + 256 * j) = o; }
;                 ss = wave_sum(ss);
;                 const float rstd = rsqrtf(ss * (1.f / DM) + EPS);
; #pragma unroll
;                 for (int j = 0; j < 4; ++j) {
;                     const f32x4 h = v[j] * rstd * mul[j] + sh[j];
;                     u32x2 o; o.x = pk2(h.x, h.y); o.y = pk2(h.z, h.w);
;                     const int c = (lane >> 1) + 32 * j;
;                     *(u32x2*)(smem + row * 2048 + ((c ^ (row & 15)) << 4) + (lane & 1) * 8) = o;
;                 }
	v_pk_fma_f32 v[52:53], v[158:159], v[52:53], v[144:145]
	v_pk_fma_f32 v[50:51], v[160:161], v[50:51], v[142:143]
	v_cvt_pk_bf16_f32 v62, v62, v63
	v_cvt_pk_bf16_f32 v63, v64, v65
	v_cvt_pk_bf16_f32 v58, v58, v59
	v_cvt_pk_bf16_f32 v59, v60, v61
	v_cvt_pk_bf16_f32 v54, v54, v55
	v_cvt_pk_bf16_f32 v55, v56, v57
	v_cvt_pk_bf16_f32 v50, v50, v51
	v_cvt_pk_bf16_f32 v51, v52, v53
	ds_write_b64 v80, v[62:63]
	ds_write_b64 v81, v[58:59]
	ds_write_b64 v82, v[54:55]
	ds_write_b64 v83, v[50:51]
	v_mul_f32_e32 v50, 0x4b800000, v66
	v_cndmask_b32_e32 v50, v66, v50, vcc
	v_rsq_f32_e32 v50, v50
	s_nop 0
	v_mul_f32_e32 v51, 0x45800000, v50
	v_cndmask_b32_e32 v50, v50, v51, vcc
	v_add_u32_e32 v51, s1, v167
	v_pk_mul_f32 v[46:47], v[46:47], v[50:51] op_sel_hi:[1,0]
	v_pk_mul_f32 v[48:49], v[48:49], v[50:51] op_sel_hi:[1,0]
	v_pk_mul_f32 v[42:43], v[42:43], v[50:51] op_sel_hi:[1,0]
	v_pk_mul_f32 v[44:45], v[44:45], v[50:51] op_sel_hi:[1,0]
	v_pk_mul_f32 v[38:39], v[38:39], v[50:51] op_sel_hi:[1,0]
	v_pk_mul_f32 v[40:41], v[40:41], v[50:51] op_sel_hi:[1,0]
	v_pk_mul_f32 v[34:35], v[34:35], v[50:51] op_sel_hi:[1,0]
	v_pk_mul_f32 v[36:37], v[36:37], v[50:51] op_sel_hi:[1,0]
	v_pk_fma_f32 v[48:49], v[146:147], v[48:49], v[132:133]
	v_pk_fma_f32 v[46:47], v[148:149], v[46:47], v[130:131]
	v_readlane_b32 s1, v255, 10
	v_pk_fma_f32 v[44:45], v[150:151], v[44:45], v[136:137]
	v_pk_fma_f32 v[42:43], v[152:153], v[42:43], v[134:135]
	v_pk_fma_f32 v[40:41], v[154:155], v[40:41], v[140:141]
	v_pk_fma_f32 v[38:39], v[156:157], v[38:39], v[138:139]
	v_pk_fma_f32 v[36:37], v[158:159], v[36:37], v[144:145]
	v_pk_fma_f32 v[34:35], v[160:161], v[34:35], v[142:143]
	v_cvt_pk_bf16_f32 v46, v46, v47
	v_cvt_pk_bf16_f32 v47, v48, v49
	v_xor_b32_e32 v48, s1, v166
	v_cvt_pk_bf16_f32 v42, v42, v43
	v_cvt_pk_bf16_f32 v43, v44, v45
	v_xor_b32_e32 v44, s1, v170
	v_cvt_pk_bf16_f32 v38, v38, v39
	v_cvt_pk_bf16_f32 v39, v40, v41
	v_xor_b32_e32 v40, s1, v169
	v_cvt_pk_bf16_f32 v34, v34, v35
	v_cvt_pk_bf16_f32 v35, v36, v37
	v_xor_b32_e32 v36, s1, v168
	v_lshl_add_u32 v48, v48, 4, v51
	v_lshl_add_u32 v44, v44, 4, v51
	v_lshl_add_u32 v40, v40, 4, v51
	v_lshl_add_u32 v36, v36, 4, v51
	ds_write_b64 v48, v[46:47]
	ds_write_b64 v44, v[42:43]
	ds_write_b64 v40, v[38:39]
	ds_write_b64 v36, v[34:35]
	v_mov_b32_e32 v36, v11
	v_mov_b32_e32 v37, v19
	v_readlane_b32 s1, v255, 12
	v_mov_b32_e32 v34, v10
	v_mov_b32_e32 v35, v18
	v_pk_mul_f32 v[36:37], v[36:37], v[36:37]
	s_add_i32 s4, s0, s1
	v_pk_fma_f32 v[34:35], v[34:35], v[34:35], v[36:37]
	v_mov_b32_e32 v36, v12
	v_mov_b32_e32 v37, v20
	s_ashr_i32 s5, s4, 31
	v_pk_fma_f32 v[34:35], v[36:37], v[36:37], v[34:35]
	v_mov_b32_e32 v36, v13
	v_mov_b32_e32 v37, v21
	s_lshl_b64 s[4:5], s[4:5], 11
	v_pk_fma_f32 v[34:35], v[36:37], v[36:37], v[34:35]
	v_lshl_add_u64 v[36:37], v[162:163], 0, s[4:5]
	v_cvt_pk_bf16_f32 v38, v30, v31
	v_cvt_pk_bf16_f32 v39, v32, v33
	global_store_dwordx2 v[36:37], v[38:39], off
	v_cvt_pk_bf16_f32 v38, v22, v23
	v_cvt_pk_bf16_f32 v39, v24, v25
	global_store_dwordx2 v[36:37], v[38:39], off offset:512
	v_cvt_pk_bf16_f32 v38, v18, v19
	v_cvt_pk_bf16_f32 v39, v20, v21
	global_store_dwordx2 v[36:37], v[38:39], off offset:1024
	v_cvt_pk_bf16_f32 v38, v10, v11
	v_cvt_pk_bf16_f32 v39, v12, v13
	global_store_dwordx2 v[36:37], v[38:39], off offset:1536
	v_mov_b32_e32 v36, v23
	v_mov_b32_e32 v37, v31
	v_pk_mul_f32 v[36:37], v[36:37], v[36:37]
	v_mov_b32_e32 v42, v22
	v_mov_b32_e32 v43, v30
	v_mov_b32_e32 v38, v24
	v_mov_b32_e32 v39, v32
	v_pk_fma_f32 v[36:37], v[42:43], v[42:43], v[36:37]
	v_mov_b32_e32 v40, v25
	v_mov_b32_e32 v41, v33
	v_pk_fma_f32 v[36:37], v[38:39], v[38:39], v[36:37]
	v_readlane_b32 s1, v255, 11
	v_pk_fma_f32 v[36:37], v[40:41], v[40:41], v[36:37]
	v_mov_b32_e32 v40, v3
	v_pk_add_f32 v[36:37], v[36:37], v[36:37] op_sel:[0,1] op_sel_hi:[1,0]
	v_mov_b32_e32 v41, v7
	v_pk_add_f32 v[36:37], v[34:35], v[36:37] op_sel:[1,0] op_sel_hi:[0,1]
	v_pk_add_f32 v[34:35], v[34:35], v[36:37]
	v_mov_b32_e32 v38, v2
	v_mov_b32_e32 v35, v34
	s_nop 1
	v_permlane16_swap_b32_e32 v34, v35
	v_add_f32_e32 v35, v34, v35
	v_add_u32_e32 v34, s1, v167
	v_readlane_b32 s1, v255, 13
	v_mov_b32_e32 v39, v6
	v_pk_mul_f32 v[40:41], v[40:41], v[40:41]
	v_xor_b32_e32 v36, s1, v166
	v_lshl_add_u32 v48, v36, 4, v34
	v_xor_b32_e32 v36, s1, v170
	v_lshl_add_u32 v49, v36, 4, v34
	v_xor_b32_e32 v36, s1, v169
	v_lshl_add_u32 v50, v36, 4, v34
	v_xor_b32_e32 v36, s1, v168
	v_readlane_b32 s1, v255, 15
	s_add_i32 s4, s0, s1
	v_pk_fma_f32 v[38:39], v[38:39], v[38:39], v[40:41]
	v_mov_b32_e32 v40, v4
	v_mov_b32_e32 v41, v8
	s_ashr_i32 s5, s4, 31
	v_pk_fma_f32 v[38:39], v[40:41], v[40:41], v[38:39]
	v_mov_b32_e32 v40, v5
	v_mov_b32_e32 v41, v9
	s_lshl_b64 s[4:5], s[4:5], 11
	v_pk_fma_f32 v[38:39], v[40:41], v[40:41], v[38:39]
	v_lshl_add_u64 v[40:41], v[162:163], 0, s[4:5]
	v_cvt_pk_bf16_f32 v42, v26, v27
	v_cvt_pk_bf16_f32 v43, v28, v29
	global_store_dwordx2 v[40:41], v[42:43], off
	v_cvt_pk_bf16_f32 v42, v14, v15
	v_cvt_pk_bf16_f32 v43, v16, v17
	global_store_dwordx2 v[40:41], v[42:43], off offset:512
	v_cvt_pk_bf16_f32 v42, v6, v7
	v_cvt_pk_bf16_f32 v43, v8, v9
	global_store_dwordx2 v[40:41], v[42:43], off offset:1024
	v_cvt_pk_bf16_f32 v42, v2, v3
	v_cvt_pk_bf16_f32 v43, v4, v5
; DEVINL unsigned pk2(float lo, float hi) { const f32x2 v = {lo, hi}; return __builtin_bit_cast(unsigned, __builtin_convertvector(v, bf16v2)); }
; DEVINL void phase2(const Params& P, unsigned char* smem, XPre& X, const bool have_pre) {
;     ...
;             for (int rr = 0; rr < 8; ++rr) {
;                 const int row = 8 * wv + rr;
;                 f32x4 v[4]; float ss = 0.f;
; #pragma unroll
;                 for (int j = 0; j < 4; ++j) { v[j] = X.v[rr][j]; ss += v[j].x * v[j].x + v[j].y * v[j].y + v[j].z * v[j].z + v[j].w * v[j].w; }
; #pragma unroll
;                 for (int j = 0; j < 4; ++j) { u32x2 o; o.x = pk2(v[j].x, v[j].y); o.y = pk2(v[j].z, v[j].w); *(u32x2*)(XB + (size_t)(m0 + row) * DM + 4 * lane + 256 * j) = o; }
;                 ss = wave_sum(ss);
;                 const float rstd = rsqrtf(ss * (1.f / DM) + EPS);
; #pragma unroll
;                 for (int j = 0; j < 4; ++j) {
;                     const f32x4 h = v[j] * rstd * mul[j] + sh[j];
;                     u32x2 o; o.x = pk2(h.x, h.y); o.y = pk2(h.z, h.w);
;                     const int c = (lane >> 1) + 32 * j;
;                     *(u32x2*)(smem + row * 2048 + ((c ^ (row & 15)) << 4) + (lane & 1) * 8) = o;
;                 }
	global_store_dwordx2 v[40:41], v[42:43], off offset:1536
	v_mov_b32_e32 v40, v15
	v_mov_b32_e32 v41, v27
	v_pk_mul_f32 v[40:41], v[40:41], v[40:41]
	v_mov_b32_e32 v46, v14
	v_mov_b32_e32 v47, v26
	v_mov_b32_e32 v42, v16
	v_mov_b32_e32 v43, v28
	v_pk_fma_f32 v[40:41], v[46:47], v[46:47], v[40:41]
	v_mov_b32_e32 v44, v17
	v_mov_b32_e32 v45, v29
	v_pk_fma_f32 v[40:41], v[42:43], v[42:43], v[40:41]
	v_lshl_add_u32 v51, v36, 4, v34
	v_pk_fma_f32 v[40:41], v[44:45], v[44:45], v[40:41]
	v_mov_b32_e32 v37, v35
	v_pk_add_f32 v[40:41], v[40:41], v[40:41] op_sel:[0,1] op_sel_hi:[1,0]
	s_nop 0
	v_permlane32_swap_b32_e32 v35, v37
	v_pk_add_f32 v[40:41], v[38:39], v[40:41] op_sel:[1,0] op_sel_hi:[0,1]
	v_pk_add_f32 v[38:39], v[38:39], v[40:41]
	v_readlane_b32 s1, v255, 14
	v_mov_b32_e32 v34, v38
	s_nop 1
	v_permlane16_swap_b32_e32 v38, v34
	v_add_f32_e32 v34, v38, v34
	v_mov_b32_e32 v36, v34
	s_nop 1
	v_permlane32_swap_b32_e32 v34, v36
	v_pk_add_f32 v[34:35], v[34:35], v[36:37]
	s_nop 1
	v_mov_b32_dpp v37, v35 quad_perm:[1,0,3,2] row_mask:0xf bank_mask:0xf bound_ctrl:1
	v_mov_b32_dpp v36, v34 quad_perm:[1,0,3,2] row_mask:0xf bank_mask:0xf bound_ctrl:1
	v_pk_add_f32 v[34:35], v[34:35], v[36:37]
	s_nop 1
	v_mov_b32_dpp v37, v35 quad_perm:[2,3,0,1] row_mask:0xf bank_mask:0xf bound_ctrl:1
	v_mov_b32_dpp v36, v34 quad_perm:[2,3,0,1] row_mask:0xf bank_mask:0xf bound_ctrl:1
	v_pk_add_f32 v[34:35], v[34:35], v[36:37]
	s_nop 1
	v_mov_b32_dpp v37, v35 row_half_mirror row_mask:0xf bank_mask:0xf bound_ctrl:1
	v_mov_b32_dpp v36, v34 row_half_mirror row_mask:0xf bank_mask:0xf bound_ctrl:1
	v_pk_add_f32 v[34:35], v[34:35], v[36:37]
	s_nop 1
	v_mov_b32_dpp v37, v35 row_mirror row_mask:0xf bank_mask:0xf bound_ctrl:1
	v_mov_b32_dpp v36, v34 row_mirror row_mask:0xf bank_mask:0xf bound_ctrl:1
	v_pk_add_f32 v[34:35], v[34:35], v[36:37]
	s_nop 0
	v_pk_fma_f32 v[34:35], v[34:35], s[10:11], v[164:165] op_sel_hi:[1,0,0]
	s_nop 0
	v_mul_f32_e32 v36, 0x4b800000, v35
	v_cmp_gt_f32_e64 s[6:7], s8, v35
	v_cmp_gt_f32_e32 vcc, s8, v34
	s_nop 0
	v_cndmask_b32_e64 v35, v35, v36, s[6:7]
	v_rsq_f32_e32 v35, v35
	s_nop 0
	v_mul_f32_e32 v36, 0x45800000, v35
	v_cndmask_b32_e64 v36, v35, v36, s[6:7]
	v_pk_mul_f32 v[30:31], v[30:31], v[36:37] op_sel_hi:[1,0]
	v_pk_mul_f32 v[32:33], v[32:33], v[36:37] op_sel_hi:[1,0]
	v_pk_mul_f32 v[22:23], v[22:23], v[36:37] op_sel_hi:[1,0]
	v_pk_mul_f32 v[24:25], v[24:25], v[36:37] op_sel_hi:[1,0]
	v_pk_mul_f32 v[18:19], v[18:19], v[36:37] op_sel_hi:[1,0]
	v_pk_mul_f32 v[20:21], v[20:21], v[36:37] op_sel_hi:[1,0]
	v_pk_mul_f32 v[10:11], v[10:11], v[36:37] op_sel_hi:[1,0]
	v_pk_mul_f32 v[12:13], v[12:13], v[36:37] op_sel_hi:[1,0]
	v_pk_fma_f32 v[32:33], v[146:147], v[32:33], v[132:133]
	v_pk_fma_f32 v[30:31], v[148:149], v[30:31], v[130:131]
	v_pk_fma_f32 v[24:25], v[150:151], v[24:25], v[136:137]
	v_pk_fma_f32 v[22:23], v[152:153], v[22:23], v[134:135]
	v_pk_fma_f32 v[20:21], v[154:155], v[20:21], v[140:141]
	v_pk_fma_f32 v[18:19], v[156:157], v[18:19], v[138:139]
	v_pk_fma_f32 v[12:13], v[158:159], v[12:13], v[144:145]
	v_pk_fma_f32 v[10:11], v[160:161], v[10:11], v[142:143]
	v_cvt_pk_bf16_f32 v30, v30, v31
	v_cvt_pk_bf16_f32 v31, v32, v33
	v_cvt_pk_bf16_f32 v22, v22, v23
	v_cvt_pk_bf16_f32 v23, v24, v25
	v_cvt_pk_bf16_f32 v18, v18, v19
	v_cvt_pk_bf16_f32 v19, v20, v21
	v_cvt_pk_bf16_f32 v10, v10, v11
	v_cvt_pk_bf16_f32 v11, v12, v13
	ds_write_b64 v48, v[30:31]
	ds_write_b64 v49, v[22:23]
	ds_write_b64 v50, v[18:19]
	ds_write_b64 v51, v[10:11]
	v_mul_f32_e32 v10, 0x4b800000, v34
	v_cndmask_b32_e32 v10, v34, v10, vcc
	v_rsq_f32_e32 v10, v10
	s_nop 0
	v_mul_f32_e32 v11, 0x45800000, v10
	v_cndmask_b32_e32 v10, v10, v11, vcc
	v_add_u32_e32 v11, s1, v167
	v_pk_mul_f32 v[12:13], v[26:27], v[10:11] op_sel_hi:[1,0]
	v_pk_mul_f32 v[18:19], v[28:29], v[10:11] op_sel_hi:[1,0]
	v_pk_fma_f32 v[12:13], v[148:149], v[12:13], v[130:131]
	v_pk_fma_f32 v[18:19], v[146:147], v[18:19], v[132:133]
	v_readlane_b32 s1, v255, 16
	v_cvt_pk_bf16_f32 v12, v12, v13
	v_cvt_pk_bf16_f32 v13, v18, v19
	v_xor_b32_e32 v18, s1, v166
	v_lshl_add_u32 v18, v18, 4, v11
	ds_write_b64 v18, v[12:13]
	v_pk_mul_f32 v[12:13], v[14:15], v[10:11] op_sel_hi:[1,0]
	v_pk_mul_f32 v[14:15], v[16:17], v[10:11] op_sel_hi:[1,0]
	v_pk_mul_f32 v[6:7], v[6:7], v[10:11] op_sel_hi:[1,0]
	v_pk_mul_f32 v[8:9], v[8:9], v[10:11] op_sel_hi:[1,0]
	v_pk_mul_f32 v[2:3], v[2:3], v[10:11] op_sel_hi:[1,0]
	v_pk_mul_f32 v[4:5], v[4:5], v[10:11] op_sel_hi:[1,0]
	v_pk_fma_f32 v[14:15], v[150:151], v[14:15], v[136:137]
	v_pk_fma_f32 v[12:13], v[152:153], v[12:13], v[134:135]
	v_pk_fma_f32 v[8:9], v[154:155], v[8:9], v[140:141]
	v_pk_fma_f32 v[6:7], v[156:157], v[6:7], v[138:139]
	v_pk_fma_f32 v[4:5], v[158:159], v[4:5], v[144:145]
	v_pk_fma_f32 v[2:3], v[160:161], v[2:3], v[142:143]
	v_cvt_pk_bf16_f32 v12, v12, v13
	v_cvt_pk_bf16_f32 v13, v14, v15
	v_xor_b32_e32 v14, s1, v170
	v_cvt_pk_bf16_f32 v6, v6, v7
	v_cvt_pk_bf16_f32 v7, v8, v9
	v_xor_b32_e32 v8, s1, v169
	v_cvt_pk_bf16_f32 v2, v2, v3
	v_cvt_pk_bf16_f32 v3, v4, v5
	v_xor_b32_e32 v4, s1, v168
	v_lshl_add_u32 v14, v14, 4, v11
	v_lshl_add_u32 v8, v8, 4, v11
	v_lshl_add_u32 v4, v4, 4, v11
	ds_write_b64 v14, v[12:13]
	ds_write_b64 v8, v[6:7]
	ds_write_b64 v4, v[2:3]

; DEVINL unsigned pk2(float lo, float hi) { const f32x2 v = {lo, hi}; return __builtin_bit_cast(unsigned, __builtin_convertvector(v, bf16v2)); }
; DEVINL float bflo(unsigned u) { return __uint_as_float(u << 16); }
; DEVINL float bfhi(unsigned u) { return __uint_as_float(u & 0xffff0000u); }
; DEVINL void phase4(const Params& P, unsigned char* smem) {
;     ...
;         __syncthreads();
;         {
;             const float* mbt = mod + (m0 >> 13) * 6144;
;             const int c2_ = 2 * t;
;             const f32x2 ga_ = *(const f32x2*)(mbt + 2048 + c2_), gp_ = *(const f32x2*)(P.g_post_mix + c2_), gf_ = *(const f32x2*)(P.g_pre_ffn + c2_), sc_ = *(const f32x2*)(mbt + 4096 + c2_), sh_ = *(const f32x2*)(mbt + 3072 + c2_);
;             *(f32x2*)(s_t1 + c2_) = ga_ * gp_; *(f32x2*)(s_t2 + c2_) = gf_ * (sc_ + 1.f); *(f32x2*)(s_t3 + c2_) = sh_;
;         }
;         {
;             const int row = t >> 3;
;             const float* sp = SSQ + (size_t)(m0 + row) * 16;
;             const f32x4 a = *(const f32x4*)sp, b2 = *(const f32x4*)(sp + 4), c2 = *(const f32x4*)(sp + 8), d2 = *(const f32x4*)(sp + 12);
;             const float rna = rsqrtf((a.x + a.y + a.z + a.w + b2.x + b2.y + b2.z + b2.w) * (1.f / 512.f) + EPS);
;             const float rsw = rsqrtf((c2.x + c2.y + c2.z + c2.w + d2.x + d2.y + d2.z + d2.w) * (1.f / 512.f) + EPS);
;             const bf16_t* src = ATT + (size_t)(m0 + row) * DM;
; #pragma unroll 8
;             for (int i = 0; i < 16; ++i) {
;                 const int c = (t & 7) + 8 * i;
;                 u32x4 v = *(const u32x4*)(src + c * 8);
;                 const float sc = (c < 64) ? rna : rsw;
;                 v.x = pk2(bflo(v.x) * sc, bfhi(v.x) * sc); v.y = pk2(bflo(v.y) * sc, bfhi(v.y) * sc);
;                 v.z = pk2(bflo(v.z) * sc, bfhi(v.z) * sc); v.w = pk2(bflo(v.w) * sc, bfhi(v.w) * sc);
;                 *(u32x4*)(smem + row * 2048 + ((c ^ (row & 15)) << 4)) = v;
;             }
;         }
.LBB0_582:
	s_lshr_b32 s0, s79, 7
	s_mulk_i32 s0, 0x1800
	s_ashr_i32 s1, s0, 31
	s_lshl_b32 s81, s79, 6
	s_lshl_b64 s[0:1], s[0:1], 2
	s_add_u32 s0, s2, s0
	s_addc_u32 s1, s3, s1
	v_lshl_add_u64 v[10:11], s[0:1], 0, v[186:187]
	v_or_b32_e32 v20, s81, v217
	v_add_co_u32_e32 v12, vcc, s69, v10
	v_ashrrev_i32_e32 v21, 31, v20
	v_lshlrev_b64 v[2:3], 6, v[20:21]
	v_addc_co_u32_e32 v13, vcc, 0, v11, vcc
	v_and_b32_e32 v190, 63, v0
	v_lshl_add_u64 v[16:17], s[16:17], 0, v[2:3]
	v_add_co_u32_e32 v10, vcc, s68, v10
	s_barrier
	global_load_dwordx4 v[2:5], v[16:17], off offset:16
	global_load_dwordx4 v[6:9], v[16:17], off offset:32
	v_addc_co_u32_e32 v11, vcc, 0, v11, vcc
	global_load_dwordx2 v[22:23], v[180:181], off
	global_load_dwordx2 v[24:25], v[12:13], off
	global_load_dwordx2 v[26:27], v[12:13], off offset:-4096
	s_nop 0
	global_load_dwordx4 v[12:15], v[16:17], off offset:48
	global_load_dwordx2 v[28:29], v[10:11], off
	s_nop 0
	global_load_dwordx4 v[16:19], v[16:17], off
	s_nop 0
	global_load_dwordx2 v[30:31], v[182:183], off
	v_lshlrev_b64 v[10:11], 11, v[20:21]
	v_lshl_add_u64 v[10:11], v[184:185], 0, v[10:11]
	global_load_dwordx4 v[130:133], v[10:11], off offset:-896
	global_load_dwordx4 v[134:137], v[10:11], off offset:-768
	global_load_dwordx4 v[138:141], v[10:11], off offset:-640
	global_load_dwordx4 v[142:145], v[10:11], off offset:-512
	global_load_dwordx4 v[146:149], v[10:11], off offset:-384
	global_load_dwordx4 v[150:153], v[10:11], off offset:-256
	global_load_dwordx4 v[154:157], v[10:11], off offset:-128
	global_load_dwordx4 v[158:161], v[10:11], off
	global_load_dwordx4 v[162:165], v[10:11], off offset:128
	global_load_dwordx4 v[166:169], v[10:11], off offset:256
	global_load_dwordx4 v[170:173], v[10:11], off offset:384
	global_load_dwordx4 v[174:177], v[10:11], off offset:512
	global_load_dwordx4 v[196:199], v[10:11], off offset:640
	global_load_dwordx4 v[200:203], v[10:11], off offset:768
	global_load_dwordx4 v[204:207], v[10:11], off offset:896
	global_load_dwordx4 v[208:211], v[10:11], off offset:1024
	s_mov_b32 s0, s25
	s_waitcnt vmcnt(24)
	v_mov_b32_e32 v33, v2
	s_waitcnt vmcnt(23)
	v_mov_b32_e32 v20, v6
	v_mov_b32_e32 v6, v8
	v_mov_b32_e32 v35, v4
	s_waitcnt vmcnt(17)
	v_mov_b32_e32 v21, v16
	v_mov_b32_e32 v16, v7
	v_mov_b32_e32 v7, v18
	v_mov_b32_e32 v18, v9
	v_pk_add_f32 v[8:9], v[20:21], v[16:17]
	v_mov_b32_e32 v32, v12
	v_pk_add_f32 v[6:7], v[6:7], v[8:9]
	v_mov_b32_e32 v2, v13
	v_pk_add_f32 v[6:7], v[18:19], v[6:7]
	v_mov_b32_e32 v34, v14
	v_pk_add_f32 v[6:7], v[32:33], v[6:7]
	v_mov_b32_e32 v4, v15
	v_pk_add_f32 v[2:3], v[2:3], v[6:7]
	v_pk_add_f32 v[12:13], v[28:29], 1.0 op_sel_hi:[1,0]
	v_pk_add_f32 v[2:3], v[34:35], v[2:3]
	v_pk_mul_f32 v[22:23], v[26:27], v[22:23]
	v_pk_add_f32 v[2:3], v[4:5], v[2:3]
	ds_write_b64 v216, v[24:25]
	v_pk_fma_f32 v[2:3], v[2:3], s[56:57], v[188:189] op_sel_hi:[1,0,0]
	ds_write_b64 v1, v[22:23]
	v_mul_f32_e32 v4, 0x4b800000, v3
	v_mul_f32_e32 v5, 0x4b800000, v2
	v_cmp_gt_f32_e32 vcc, s70, v3
	v_cmp_gt_f32_e64 s[8:9], s70, v2
	s_nop 0
	v_cndmask_b32_e32 v3, v3, v4, vcc
	v_cndmask_b32_e64 v2, v2, v5, s[8:9]
	v_rsq_f32_e32 v4, v3
	v_rsq_f32_e32 v5, v2
	s_waitcnt vmcnt(16)
	v_pk_mul_f32 v[2:3], v[30:31], v[12:13]
	ds_write_b64 v189, v[2:3]
	v_mul_f32_e32 v2, 0x45800000, v4
	v_mul_f32_e32 v3, 0x45800000, v5
	v_cndmask_b32_e32 v12, v4, v2, vcc
	v_cndmask_b32_e64 v13, v5, v3, s[8:9]
.LBB0_583:
	s_waitcnt vmcnt(8)
	v_mov_b32_e32 v2, v130
	v_mov_b32_e32 v3, v131
	v_mov_b32_e32 v4, v132
	v_mov_b32_e32 v5, v133
	v_mov_b32_e32 v6, v134
	v_mov_b32_e32 v7, v135
	v_mov_b32_e32 v8, v136
	v_mov_b32_e32 v9, v137
	v_mov_b32_e32 v14, v138
	v_mov_b32_e32 v15, v139
	v_mov_b32_e32 v16, v140
	v_mov_b32_e32 v17, v141
	v_mov_b32_e32 v18, v142
	v_mov_b32_e32 v19, v143
	v_mov_b32_e32 v20, v144
	v_mov_b32_e32 v21, v145
	v_mov_b32_e32 v22, v146
	v_mov_b32_e32 v23, v147
	v_mov_b32_e32 v24, v148
	v_mov_b32_e32 v25, v149
	v_mov_b32_e32 v26, v150
	v_mov_b32_e32 v27, v151
	v_mov_b32_e32 v28, v152
	v_mov_b32_e32 v29, v153
	v_mov_b32_e32 v30, v154
	v_mov_b32_e32 v31, v155
	v_mov_b32_e32 v32, v156
	v_mov_b32_e32 v33, v157
	v_mov_b32_e32 v34, v158
	v_mov_b32_e32 v35, v159
	v_mov_b32_e32 v36, v160
	v_mov_b32_e32 v37, v161
	v_add_u32_e32 v39, s0, v218
	s_cmp_eq_u32 s0, 0
	v_xor_b32_e32 v40, v39, v220
	v_add_u32_e32 v41, 8, v39
	v_add_u32_e32 v42, 16, v39
	v_add_u32_e32 v43, 24, v39
	v_add_u32_e32 v44, 32, v39
	s_cselect_b64 vcc, -1, 0
	v_add_u32_e32 v45, 40, v39
	v_add_u32_e32 v46, 48, v39
	v_add_u32_e32 v39, 56, v39
	v_lshl_add_u32 v102, v40, 4, v219
	v_xor_b32_e32 v40, v41, v220
	v_xor_b32_e32 v41, v42, v220
	v_xor_b32_e32 v42, v43, v220
	v_xor_b32_e32 v43, v44, v220
	v_cndmask_b32_e32 v38, v13, v12, vcc
	v_xor_b32_e32 v44, v45, v220
	v_xor_b32_e32 v45, v46, v220
	v_xor_b32_e32 v39, v39, v220
	v_lshl_add_u32 v103, v40, 4, v219
	v_lshl_add_u32 v104, v41, 4, v219
	v_lshl_add_u32 v105, v42, 4, v219
	v_lshl_add_u32 v106, v43, 4, v219
	s_add_i32 s0, s0, 64
	v_lshl_add_u32 v107, v44, 4, v219
	v_lshl_add_u32 v108, v45, 4, v219
	v_lshl_add_u64 v[10:11], v[10:11], 0, s[58:59]
	s_cmpk_eq_i32 s0, 0x80
	v_lshl_add_u32 v109, v39, 4, v219
	v_lshlrev_b32_e32 v40, 16, v2
	v_and_b32_e32 v41, 0xffff0000, v2
	v_lshlrev_b32_e32 v2, 16, v3
	v_and_b32_e32 v3, 0xffff0000, v3
	v_lshlrev_b32_e32 v42, 16, v4
	v_and_b32_e32 v43, 0xffff0000, v4
	v_lshlrev_b32_e32 v4, 16, v5
	v_and_b32_e32 v5, 0xffff0000, v5
	v_lshlrev_b32_e32 v44, 16, v6
	v_and_b32_e32 v45, 0xffff0000, v6
	v_lshlrev_b32_e32 v6, 16, v7
	v_and_b32_e32 v7, 0xffff0000, v7
	v_lshlrev_b32_e32 v46, 16, v8
	v_and_b32_e32 v47, 0xffff0000, v8
	v_lshlrev_b32_e32 v8, 16, v9
; DEVINL unsigned pk2(float lo, float hi) { const f32x2 v = {lo, hi}; return __builtin_bit_cast(unsigned, __builtin_convertvector(v, bf16v2)); }
; DEVINL float bflo(unsigned u) { return __uint_as_float(u << 16); }
; DEVINL float bfhi(unsigned u) { return __uint_as_float(u & 0xffff0000u); }
; DEVINL void phase4(const Params& P, unsigned char* smem) {
;     ...
;             for (int i = 0; i < 16; ++i) {
;                 const int c = (t & 7) + 8 * i;
;                 u32x4 v = *(const u32x4*)(src + c * 8);
;                 const float sc = (c < 64) ? rna : rsw;
;                 v.x = pk2(bflo(v.x) * sc, bfhi(v.x) * sc); v.y = pk2(bflo(v.y) * sc, bfhi(v.y) * sc);
;                 v.z = pk2(bflo(v.z) * sc, bfhi(v.z) * sc); v.w = pk2(bflo(v.w) * sc, bfhi(v.w) * sc);
;                 *(u32x4*)(smem + row * 2048 + ((c ^ (row & 15)) << 4)) = v;
;             }
	v_and_b32_e32 v9, 0xffff0000, v9
	v_lshlrev_b32_e32 v48, 16, v14
	v_and_b32_e32 v49, 0xffff0000, v14
	v_lshlrev_b32_e32 v14, 16, v15
	v_and_b32_e32 v15, 0xffff0000, v15
	v_lshlrev_b32_e32 v50, 16, v16
	v_and_b32_e32 v51, 0xffff0000, v16
	v_lshlrev_b32_e32 v16, 16, v17
	v_and_b32_e32 v17, 0xffff0000, v17
	v_lshlrev_b32_e32 v52, 16, v18
	v_and_b32_e32 v53, 0xffff0000, v18
	v_lshlrev_b32_e32 v18, 16, v19
	v_and_b32_e32 v19, 0xffff0000, v19
	v_lshlrev_b32_e32 v54, 16, v20
	v_and_b32_e32 v55, 0xffff0000, v20
	v_lshlrev_b32_e32 v20, 16, v21
	v_and_b32_e32 v21, 0xffff0000, v21
	v_lshlrev_b32_e32 v56, 16, v22
	v_and_b32_e32 v57, 0xffff0000, v22
	v_lshlrev_b32_e32 v22, 16, v23
	v_and_b32_e32 v23, 0xffff0000, v23
	v_lshlrev_b32_e32 v58, 16, v24
	v_and_b32_e32 v59, 0xffff0000, v24
	v_lshlrev_b32_e32 v24, 16, v25
	v_and_b32_e32 v25, 0xffff0000, v25
	v_lshlrev_b32_e32 v60, 16, v26
	v_and_b32_e32 v61, 0xffff0000, v26
	v_lshlrev_b32_e32 v26, 16, v27
	v_and_b32_e32 v27, 0xffff0000, v27
	v_lshlrev_b32_e32 v62, 16, v28
	v_and_b32_e32 v63, 0xffff0000, v28
	v_lshlrev_b32_e32 v28, 16, v29
	v_and_b32_e32 v29, 0xffff0000, v29
	v_lshlrev_b32_e32 v64, 16, v30
	v_and_b32_e32 v65, 0xffff0000, v30
	v_lshlrev_b32_e32 v30, 16, v31
	v_and_b32_e32 v31, 0xffff0000, v31
	v_lshlrev_b32_e32 v66, 16, v32
	v_and_b32_e32 v67, 0xffff0000, v32
	v_lshlrev_b32_e32 v32, 16, v33
	v_and_b32_e32 v33, 0xffff0000, v33
	v_lshlrev_b32_e32 v68, 16, v34
	v_and_b32_e32 v69, 0xffff0000, v34
	v_lshlrev_b32_e32 v34, 16, v35
	v_and_b32_e32 v35, 0xffff0000, v35
	v_lshlrev_b32_e32 v70, 16, v36
	v_and_b32_e32 v71, 0xffff0000, v36
	v_lshlrev_b32_e32 v36, 16, v37
	v_and_b32_e32 v37, 0xffff0000, v37
	v_pk_mul_f32 v[40:41], v[38:39], v[40:41] op_sel_hi:[0,1]
	v_pk_mul_f32 v[72:73], v[38:39], v[2:3] op_sel_hi:[0,1]
	v_pk_mul_f32 v[42:43], v[38:39], v[42:43] op_sel_hi:[0,1]
	v_pk_mul_f32 v[74:75], v[38:39], v[4:5] op_sel_hi:[0,1]
	v_pk_mul_f32 v[44:45], v[38:39], v[44:45] op_sel_hi:[0,1]
	v_pk_mul_f32 v[76:77], v[38:39], v[6:7] op_sel_hi:[0,1]
	v_pk_mul_f32 v[46:47], v[38:39], v[46:47] op_sel_hi:[0,1]
	v_pk_mul_f32 v[78:79], v[38:39], v[8:9] op_sel_hi:[0,1]
	v_pk_mul_f32 v[48:49], v[38:39], v[48:49] op_sel_hi:[0,1]
	v_pk_mul_f32 v[80:81], v[38:39], v[14:15] op_sel_hi:[0,1]
	v_pk_mul_f32 v[50:51], v[38:39], v[50:51] op_sel_hi:[0,1]
	v_pk_mul_f32 v[82:83], v[38:39], v[16:17] op_sel_hi:[0,1]
	v_pk_mul_f32 v[52:53], v[38:39], v[52:53] op_sel_hi:[0,1]
	v_pk_mul_f32 v[84:85], v[38:39], v[18:19] op_sel_hi:[0,1]
	v_pk_mul_f32 v[54:55], v[38:39], v[54:55] op_sel_hi:[0,1]
	v_pk_mul_f32 v[86:87], v[38:39], v[20:21] op_sel_hi:[0,1]
	v_pk_mul_f32 v[56:57], v[38:39], v[56:57] op_sel_hi:[0,1]
	v_pk_mul_f32 v[88:89], v[38:39], v[22:23] op_sel_hi:[0,1]
	v_pk_mul_f32 v[58:59], v[38:39], v[58:59] op_sel_hi:[0,1]
	v_pk_mul_f32 v[90:91], v[38:39], v[24:25] op_sel_hi:[0,1]
	v_pk_mul_f32 v[60:61], v[38:39], v[60:61] op_sel_hi:[0,1]
	v_pk_mul_f32 v[92:93], v[38:39], v[26:27] op_sel_hi:[0,1]
	v_pk_mul_f32 v[62:63], v[38:39], v[62:63] op_sel_hi:[0,1]
	v_pk_mul_f32 v[94:95], v[38:39], v[28:29] op_sel_hi:[0,1]
	v_pk_mul_f32 v[64:65], v[38:39], v[64:65] op_sel_hi:[0,1]
	v_pk_mul_f32 v[96:97], v[38:39], v[30:31] op_sel_hi:[0,1]
	v_pk_mul_f32 v[66:67], v[38:39], v[66:67] op_sel_hi:[0,1]
	v_pk_mul_f32 v[98:99], v[38:39], v[32:33] op_sel_hi:[0,1]
	v_pk_mul_f32 v[68:69], v[38:39], v[68:69] op_sel_hi:[0,1]
	v_pk_mul_f32 v[100:101], v[38:39], v[34:35] op_sel_hi:[0,1]
	v_pk_mul_f32 v[70:71], v[38:39], v[70:71] op_sel_hi:[0,1]
	v_pk_mul_f32 v[38:39], v[38:39], v[36:37] op_sel_hi:[0,1]
	v_cvt_pk_bf16_f32 v2, v40, v41
	v_cvt_pk_bf16_f32 v3, v72, v73
	v_cvt_pk_bf16_f32 v4, v42, v43
	v_cvt_pk_bf16_f32 v5, v74, v75
	v_cvt_pk_bf16_f32 v6, v44, v45
	v_cvt_pk_bf16_f32 v7, v76, v77
	v_cvt_pk_bf16_f32 v8, v46, v47
	v_cvt_pk_bf16_f32 v9, v78, v79
	v_cvt_pk_bf16_f32 v14, v48, v49
	v_cvt_pk_bf16_f32 v15, v80, v81
	v_cvt_pk_bf16_f32 v16, v50, v51
	v_cvt_pk_bf16_f32 v17, v82, v83
	v_cvt_pk_bf16_f32 v18, v52, v53
	v_cvt_pk_bf16_f32 v19, v84, v85
	v_cvt_pk_bf16_f32 v20, v54, v55
	v_cvt_pk_bf16_f32 v21, v86, v87
	v_cvt_pk_bf16_f32 v22, v56, v57
	v_cvt_pk_bf16_f32 v23, v88, v89
	v_cvt_pk_bf16_f32 v24, v58, v59
	v_cvt_pk_bf16_f32 v25, v90, v91
	v_cvt_pk_bf16_f32 v26, v60, v61
	v_cvt_pk_bf16_f32 v27, v92, v93
	v_cvt_pk_bf16_f32 v28, v62, v63
	v_cvt_pk_bf16_f32 v29, v94, v95
	v_cvt_pk_bf16_f32 v30, v64, v65
	v_cvt_pk_bf16_f32 v31, v96, v97
	v_cvt_pk_bf16_f32 v32, v66, v67
	v_cvt_pk_bf16_f32 v33, v98, v99
	v_cvt_pk_bf16_f32 v34, v68, v69
	v_cvt_pk_bf16_f32 v35, v100, v101
	v_cvt_pk_bf16_f32 v36, v70, v71
	v_cvt_pk_bf16_f32 v37, v38, v39
	ds_write_b128 v102, v[2:5]
	ds_write_b128 v103, v[6:9]
	ds_write_b128 v104, v[14:17]
	ds_write_b128 v105, v[18:21]
	ds_write_b128 v106, v[22:25]
	ds_write_b128 v107, v[26:29]
	ds_write_b128 v108, v[30:33]
	ds_write_b128 v109, v[34:37]
	s_waitcnt vmcnt(0)
; DEVINL unsigned pk2(float lo, float hi) { const f32x2 v = {lo, hi}; return __builtin_bit_cast(unsigned, __builtin_convertvector(v, bf16v2)); }
; DEVINL float bflo(unsigned u) { return __uint_as_float(u << 16); }
; DEVINL float bfhi(unsigned u) { return __uint_as_float(u & 0xffff0000u); }
; DEVINL void phase4(const Params& P, unsigned char* smem) {
;     ...
;             for (int i = 0; i < 16; ++i) {
;                 const int c = (t & 7) + 8 * i;
;                 u32x4 v = *(const u32x4*)(src + c * 8);
;                 const float sc = (c < 64) ? rna : rsw;
;                 v.x = pk2(bflo(v.x) * sc, bfhi(v.x) * sc); v.y = pk2(bflo(v.y) * sc, bfhi(v.y) * sc);
;                 v.z = pk2(bflo(v.z) * sc, bfhi(v.z) * sc); v.w = pk2(bflo(v.w) * sc, bfhi(v.w) * sc);
;                 *(u32x4*)(smem + row * 2048 + ((c ^ (row & 15)) << 4)) = v;
;             }
	v_mov_b32_e32 v2, v162
	v_mov_b32_e32 v3, v163
	v_mov_b32_e32 v4, v164
	v_mov_b32_e32 v5, v165
	v_mov_b32_e32 v6, v166
	v_mov_b32_e32 v7, v167
	v_mov_b32_e32 v8, v168
	v_mov_b32_e32 v9, v169
	v_mov_b32_e32 v14, v170
	v_mov_b32_e32 v15, v171
	v_mov_b32_e32 v16, v172
	v_mov_b32_e32 v17, v173
	v_mov_b32_e32 v18, v174
	v_mov_b32_e32 v19, v175
	v_mov_b32_e32 v20, v176
	v_mov_b32_e32 v21, v177
	v_mov_b32_e32 v22, v196
	v_mov_b32_e32 v23, v197
	v_mov_b32_e32 v24, v198
	v_mov_b32_e32 v25, v199
	v_mov_b32_e32 v26, v200
	v_mov_b32_e32 v27, v201
	v_mov_b32_e32 v28, v202
	v_mov_b32_e32 v29, v203
	v_mov_b32_e32 v30, v204
	v_mov_b32_e32 v31, v205
	v_mov_b32_e32 v32, v206
	v_mov_b32_e32 v33, v207
	v_mov_b32_e32 v34, v208
	v_mov_b32_e32 v35, v209
	v_mov_b32_e32 v36, v210
	v_mov_b32_e32 v37, v211
	v_add_u32_e32 v39, s0, v218
	s_cmp_eq_u32 s0, 0
	v_xor_b32_e32 v40, v39, v220
	v_add_u32_e32 v41, 8, v39
	v_add_u32_e32 v42, 16, v39
	v_add_u32_e32 v43, 24, v39
	v_add_u32_e32 v44, 32, v39
	s_cselect_b64 vcc, -1, 0
	v_add_u32_e32 v45, 40, v39
	v_add_u32_e32 v46, 48, v39
	v_add_u32_e32 v39, 56, v39
	v_lshl_add_u32 v102, v40, 4, v219
	v_xor_b32_e32 v40, v41, v220
	v_xor_b32_e32 v41, v42, v220
	v_xor_b32_e32 v42, v43, v220
	v_xor_b32_e32 v43, v44, v220
	v_cndmask_b32_e32 v38, v13, v12, vcc
	v_xor_b32_e32 v44, v45, v220
	v_xor_b32_e32 v45, v46, v220
	v_xor_b32_e32 v39, v39, v220
	v_lshl_add_u32 v103, v40, 4, v219
	v_lshl_add_u32 v104, v41, 4, v219
	v_lshl_add_u32 v105, v42, 4, v219
	v_lshl_add_u32 v106, v43, 4, v219
	s_add_i32 s0, s0, 64
	v_lshl_add_u32 v107, v44, 4, v219
	v_lshl_add_u32 v108, v45, 4, v219
	v_lshl_add_u64 v[10:11], v[10:11], 0, s[58:59]
	s_cmpk_eq_i32 s0, 0x80
	v_lshl_add_u32 v109, v39, 4, v219
	v_lshlrev_b32_e32 v40, 16, v2
	v_and_b32_e32 v41, 0xffff0000, v2
	v_lshlrev_b32_e32 v2, 16, v3
	v_and_b32_e32 v3, 0xffff0000, v3
	v_lshlrev_b32_e32 v42, 16, v4
	v_and_b32_e32 v43, 0xffff0000, v4
	v_lshlrev_b32_e32 v4, 16, v5
	v_and_b32_e32 v5, 0xffff0000, v5
	v_lshlrev_b32_e32 v44, 16, v6
	v_and_b32_e32 v45, 0xffff0000, v6
	v_lshlrev_b32_e32 v6, 16, v7
	v_and_b32_e32 v7, 0xffff0000, v7
	v_lshlrev_b32_e32 v46, 16, v8
	v_and_b32_e32 v47, 0xffff0000, v8
	v_lshlrev_b32_e32 v8, 16, v9
	v_and_b32_e32 v9, 0xffff0000, v9
	v_lshlrev_b32_e32 v48, 16, v14
	v_and_b32_e32 v49, 0xffff0000, v14
	v_lshlrev_b32_e32 v14, 16, v15
	v_and_b32_e32 v15, 0xffff0000, v15
	v_lshlrev_b32_e32 v50, 16, v16
	v_and_b32_e32 v51, 0xffff0000, v16
	v_lshlrev_b32_e32 v16, 16, v17
	v_and_b32_e32 v17, 0xffff0000, v17
	v_lshlrev_b32_e32 v52, 16, v18
	v_and_b32_e32 v53, 0xffff0000, v18
	v_lshlrev_b32_e32 v18, 16, v19
	v_and_b32_e32 v19, 0xffff0000, v19
	v_lshlrev_b32_e32 v54, 16, v20
	v_and_b32_e32 v55, 0xffff0000, v20
	v_lshlrev_b32_e32 v20, 16, v21
	v_and_b32_e32 v21, 0xffff0000, v21
	v_lshlrev_b32_e32 v56, 16, v22
	v_and_b32_e32 v57, 0xffff0000, v22
	v_lshlrev_b32_e32 v22, 16, v23
	v_and_b32_e32 v23, 0xffff0000, v23
	v_lshlrev_b32_e32 v58, 16, v24
	v_and_b32_e32 v59, 0xffff0000, v24
	v_lshlrev_b32_e32 v24, 16, v25
	v_and_b32_e32 v25, 0xffff0000, v25
	v_lshlrev_b32_e32 v60, 16, v26
	v_and_b32_e32 v61, 0xffff0000, v26
	v_lshlrev_b32_e32 v26, 16, v27
	v_and_b32_e32 v27, 0xffff0000, v27
	v_lshlrev_b32_e32 v62, 16, v28
	v_and_b32_e32 v63, 0xffff0000, v28
	v_lshlrev_b32_e32 v28, 16, v29
	v_and_b32_e32 v29, 0xffff0000, v29
	v_lshlrev_b32_e32 v64, 16, v30
	v_and_b32_e32 v65, 0xffff0000, v30
	v_lshlrev_b32_e32 v30, 16, v31
	v_and_b32_e32 v31, 0xffff0000, v31
	v_lshlrev_b32_e32 v66, 16, v32
	v_and_b32_e32 v67, 0xffff0000, v32
	v_lshlrev_b32_e32 v32, 16, v33
	v_and_b32_e32 v33, 0xffff0000, v33
	v_lshlrev_b32_e32 v68, 16, v34
	v_and_b32_e32 v69, 0xffff0000, v34
	v_lshlrev_b32_e32 v34, 16, v35
	v_and_b32_e32 v35, 0xffff0000, v35
	v_lshlrev_b32_e32 v70, 16, v36
	v_and_b32_e32 v71, 0xffff0000, v36
	v_lshlrev_b32_e32 v36, 16, v37
	v_and_b32_e32 v37, 0xffff0000, v37
	v_pk_mul_f32 v[40:41], v[38:39], v[40:41] op_sel_hi:[0,1]
	v_pk_mul_f32 v[72:73], v[38:39], v[2:3] op_sel_hi:[0,1]
	v_pk_mul_f32 v[42:43], v[38:39], v[42:43] op_sel_hi:[0,1]
	v_pk_mul_f32 v[74:75], v[38:39], v[4:5] op_sel_hi:[0,1]
	v_pk_mul_f32 v[44:45], v[38:39], v[44:45] op_sel_hi:[0,1]
	v_pk_mul_f32 v[76:77], v[38:39], v[6:7] op_sel_hi:[0,1]
	v_pk_mul_f32 v[46:47], v[38:39], v[46:47] op_sel_hi:[0,1]
	v_pk_mul_f32 v[78:79], v[38:39], v[8:9] op_sel_hi:[0,1]
	v_pk_mul_f32 v[48:49], v[38:39], v[48:49] op_sel_hi:[0,1]
	v_pk_mul_f32 v[80:81], v[38:39], v[14:15] op_sel_hi:[0,1]
	v_pk_mul_f32 v[50:51], v[38:39], v[50:51] op_sel_hi:[0,1]
	v_pk_mul_f32 v[82:83], v[38:39], v[16:17] op_sel_hi:[0,1]
	v_pk_mul_f32 v[52:53], v[38:39], v[52:53] op_sel_hi:[0,1]
	v_pk_mul_f32 v[84:85], v[38:39], v[18:19] op_sel_hi:[0,1]
	v_pk_mul_f32 v[54:55], v[38:39], v[54:55] op_sel_hi:[0,1]
	v_pk_mul_f32 v[86:87], v[38:39], v[20:21] op_sel_hi:[0,1]
	v_pk_mul_f32 v[56:57], v[38:39], v[56:57] op_sel_hi:[0,1]
	v_pk_mul_f32 v[88:89], v[38:39], v[22:23] op_sel_hi:[0,1]
	v_pk_mul_f32 v[58:59], v[38:39], v[58:59] op_sel_hi:[0,1]
	v_pk_mul_f32 v[90:91], v[38:39], v[24:25] op_sel_hi:[0,1]
	v_pk_mul_f32 v[60:61], v[38:39], v[60:61] op_sel_hi:[0,1]
	v_pk_mul_f32 v[92:93], v[38:39], v[26:27] op_sel_hi:[0,1]
	v_pk_mul_f32 v[62:63], v[38:39], v[62:63] op_sel_hi:[0,1]
	v_pk_mul_f32 v[94:95], v[38:39], v[28:29] op_sel_hi:[0,1]
	v_pk_mul_f32 v[64:65], v[38:39], v[64:65] op_sel_hi:[0,1]
	v_pk_mul_f32 v[96:97], v[38:39], v[30:31] op_sel_hi:[0,1]
	v_pk_mul_f32 v[66:67], v[38:39], v[66:67] op_sel_hi:[0,1]
	v_pk_mul_f32 v[98:99], v[38:39], v[32:33] op_sel_hi:[0,1]
	v_pk_mul_f32 v[68:69], v[38:39], v[68:69] op_sel_hi:[0,1]
	v_pk_mul_f32 v[100:101], v[38:39], v[34:35] op_sel_hi:[0,1]
; DEVINL unsigned pk2(float lo, float hi) { const f32x2 v = {lo, hi}; return __builtin_bit_cast(unsigned, __builtin_convertvector(v, bf16v2)); }
; DEVINL float bflo(unsigned u) { return __uint_as_float(u << 16); }
; DEVINL float bfhi(unsigned u) { return __uint_as_float(u & 0xffff0000u); }
; DEVINL void phase4(const Params& P, unsigned char* smem) {
;     ...
;             for (int i = 0; i < 16; ++i) {
;                 const int c = (t & 7) + 8 * i;
;                 u32x4 v = *(const u32x4*)(src + c * 8);
;                 const float sc = (c < 64) ? rna : rsw;
;                 v.x = pk2(bflo(v.x) * sc, bfhi(v.x) * sc); v.y = pk2(bflo(v.y) * sc, bfhi(v.y) * sc);
;                 v.z = pk2(bflo(v.z) * sc, bfhi(v.z) * sc); v.w = pk2(bflo(v.w) * sc, bfhi(v.w) * sc);
;                 *(u32x4*)(smem + row * 2048 + ((c ^ (row & 15)) << 4)) = v;
;             }
;         }
;         __syncthreads();
;         f32x4 acc[8][4];
; #pragma unroll
;         for (int i = 0; i < 8; ++i)
; #pragma unroll
;             for (int mi = 0; mi < 4; ++mi) acc[i][mi] = (f32x4){0.f, 0.f, 0.f, 0.f};
	v_pk_mul_f32 v[70:71], v[38:39], v[70:71] op_sel_hi:[0,1]
	v_pk_mul_f32 v[38:39], v[38:39], v[36:37] op_sel_hi:[0,1]
	v_cvt_pk_bf16_f32 v2, v40, v41
	v_cvt_pk_bf16_f32 v3, v72, v73
	v_cvt_pk_bf16_f32 v4, v42, v43
	v_cvt_pk_bf16_f32 v5, v74, v75
	v_cvt_pk_bf16_f32 v6, v44, v45
	v_cvt_pk_bf16_f32 v7, v76, v77
	v_cvt_pk_bf16_f32 v8, v46, v47
	v_cvt_pk_bf16_f32 v9, v78, v79
	v_cvt_pk_bf16_f32 v14, v48, v49
	v_cvt_pk_bf16_f32 v15, v80, v81
	v_cvt_pk_bf16_f32 v16, v50, v51
	v_cvt_pk_bf16_f32 v17, v82, v83
	v_cvt_pk_bf16_f32 v18, v52, v53
	v_cvt_pk_bf16_f32 v19, v84, v85
	v_cvt_pk_bf16_f32 v20, v54, v55
	v_cvt_pk_bf16_f32 v21, v86, v87
	v_cvt_pk_bf16_f32 v22, v56, v57
	v_cvt_pk_bf16_f32 v23, v88, v89
	v_cvt_pk_bf16_f32 v24, v58, v59
	v_cvt_pk_bf16_f32 v25, v90, v91
	v_cvt_pk_bf16_f32 v26, v60, v61
	v_cvt_pk_bf16_f32 v27, v92, v93
	v_cvt_pk_bf16_f32 v28, v62, v63
	v_cvt_pk_bf16_f32 v29, v94, v95
	v_cvt_pk_bf16_f32 v30, v64, v65
	v_cvt_pk_bf16_f32 v31, v96, v97
	v_cvt_pk_bf16_f32 v32, v66, v67
	v_cvt_pk_bf16_f32 v33, v98, v99
	v_cvt_pk_bf16_f32 v34, v68, v69
	v_cvt_pk_bf16_f32 v35, v100, v101
	v_cvt_pk_bf16_f32 v36, v70, v71
	v_cvt_pk_bf16_f32 v37, v38, v39
	ds_write_b128 v102, v[2:5]
	ds_write_b128 v103, v[6:9]
	ds_write_b128 v104, v[14:17]
	ds_write_b128 v105, v[18:21]
	ds_write_b128 v106, v[22:25]
	ds_write_b128 v107, v[26:29]
	ds_write_b128 v108, v[30:33]
	ds_write_b128 v109, v[34:37]
	v_mov_b32_e32 v5, 0
	v_and_b32_e32 v238, 15, v190
	v_ashrrev_i32_e32 v204, 4, v190
	s_and_b64 vcc, exec, s[42:43]
	v_mov_b32_e32 v4, v5
	v_mov_b32_e32 v3, v5
	v_mov_b32_e32 v2, v5
	v_mov_b32_e32 v9, v5
	v_mov_b32_e32 v8, v5
	v_mov_b32_e32 v7, v5
	v_mov_b32_e32 v6, v5
	v_mov_b32_e32 v69, v5
	v_mov_b32_e32 v68, v5
	v_mov_b32_e32 v67, v5
	v_mov_b32_e32 v66, v5
	v_mov_b32_e32 v73, v5
	v_mov_b32_e32 v72, v5
	v_mov_b32_e32 v71, v5
	v_mov_b32_e32 v70, v5
	v_mov_b32_e32 v13, v5
	v_mov_b32_e32 v12, v5
	v_mov_b32_e32 v11, v5
	v_mov_b32_e32 v10, v5
	v_mov_b32_e32 v17, v5
	v_mov_b32_e32 v16, v5
	v_mov_b32_e32 v15, v5
	v_mov_b32_e32 v14, v5
	v_mov_b32_e32 v77, v5
	v_mov_b32_e32 v76, v5
	v_mov_b32_e32 v75, v5
	v_mov_b32_e32 v74, v5
	v_mov_b32_e32 v81, v5
	v_mov_b32_e32 v80, v5
	v_mov_b32_e32 v79, v5
	v_mov_b32_e32 v78, v5
	v_mov_b32_e32 v21, v5
	v_mov_b32_e32 v20, v5
	v_mov_b32_e32 v19, v5
	v_mov_b32_e32 v18, v5
	v_mov_b32_e32 v25, v5
	v_mov_b32_e32 v24, v5
	v_mov_b32_e32 v23, v5
	v_mov_b32_e32 v22, v5
	v_mov_b32_e32 v85, v5
	v_mov_b32_e32 v84, v5
	v_mov_b32_e32 v83, v5
	v_mov_b32_e32 v82, v5
	v_mov_b32_e32 v89, v5
	v_mov_b32_e32 v88, v5
	v_mov_b32_e32 v87, v5
	v_mov_b32_e32 v86, v5
	v_mov_b32_e32 v29, v5
	v_mov_b32_e32 v28, v5
	v_mov_b32_e32 v27, v5
	v_mov_b32_e32 v26, v5
	v_mov_b32_e32 v33, v5
	v_mov_b32_e32 v32, v5
	v_mov_b32_e32 v31, v5
	v_mov_b32_e32 v30, v5
	v_mov_b32_e32 v93, v5
	v_mov_b32_e32 v92, v5
	v_mov_b32_e32 v91, v5
	v_mov_b32_e32 v90, v5
	v_mov_b32_e32 v97, v5
	v_mov_b32_e32 v96, v5
	v_mov_b32_e32 v95, v5
	v_mov_b32_e32 v94, v5
	v_mov_b32_e32 v129, v5
	v_mov_b32_e32 v128, v5
	v_mov_b32_e32 v127, v5
	v_mov_b32_e32 v126, v5
	v_mov_b32_e32 v125, v5
	v_mov_b32_e32 v124, v5
	v_mov_b32_e32 v123, v5
	v_mov_b32_e32 v122, v5
	v_mov_b32_e32 v65, v5
	v_mov_b32_e32 v64, v5
	v_mov_b32_e32 v63, v5
	v_mov_b32_e32 v62, v5
	v_mov_b32_e32 v61, v5
	v_mov_b32_e32 v60, v5
	v_mov_b32_e32 v59, v5
	v_mov_b32_e32 v58, v5
	v_mov_b32_e32 v121, v5
	v_mov_b32_e32 v120, v5
	v_mov_b32_e32 v119, v5
	v_mov_b32_e32 v118, v5
	v_mov_b32_e32 v117, v5
	v_mov_b32_e32 v116, v5
	v_mov_b32_e32 v115, v5
	v_mov_b32_e32 v114, v5
	v_mov_b32_e32 v57, v5
	v_mov_b32_e32 v56, v5
	v_mov_b32_e32 v55, v5
	v_mov_b32_e32 v54, v5
	v_mov_b32_e32 v53, v5
	v_mov_b32_e32 v52, v5
	v_mov_b32_e32 v51, v5
	v_mov_b32_e32 v50, v5
	v_mov_b32_e32 v113, v5
	v_mov_b32_e32 v112, v5
	v_mov_b32_e32 v111, v5
	v_mov_b32_e32 v110, v5
	v_mov_b32_e32 v109, v5
	v_mov_b32_e32 v108, v5
	v_mov_b32_e32 v107, v5
	v_mov_b32_e32 v106, v5
	v_mov_b32_e32 v49, v5
	v_mov_b32_e32 v48, v5
	v_mov_b32_e32 v47, v5
	v_mov_b32_e32 v46, v5
	v_mov_b32_e32 v45, v5
	v_mov_b32_e32 v44, v5
	v_mov_b32_e32 v43, v5
	v_mov_b32_e32 v42, v5
	v_mov_b32_e32 v105, v5
	v_mov_b32_e32 v104, v5
	v_mov_b32_e32 v103, v5
	v_mov_b32_e32 v102, v5
	v_mov_b32_e32 v101, v5
	v_mov_b32_e32 v100, v5
	v_mov_b32_e32 v99, v5
	v_mov_b32_e32 v98, v5
	v_mov_b32_e32 v41, v5
	v_mov_b32_e32 v40, v5
	v_mov_b32_e32 v39, v5
	v_mov_b32_e32 v38, v5
	v_mov_b32_e32 v37, v5
	v_mov_b32_e32 v36, v5
	v_mov_b32_e32 v35, v5
	v_mov_b32_e32 v34, v5
	s_waitcnt lgkmcnt(0)
	s_barrier
; #define LOADB(dst, ks_) do { const unsigned char* ub_ = wb + (size_t)((ks_) * 144) * 1024; \
;         _Pragma("unroll") for (int j_ = 0; j_ < 8; ++j_) dst[j_] = *(const bf16x8*)(ub_ + j_ * 1024 + voff); } while (0)
; #define LOADA(fd, ks_) do { _Pragma("unroll") for (int mi_ = 0; mi_ < 4; ++mi_) fd[mi_] = AFRAG(mi_, ks_); } while (0)
; #define LOADB(dst, ks_) do { const unsigned char* ub_ = wb + (size_t)((ks_) * 64) * 1024; \
;         _Pragma("unroll") for (int j_ = 0; j_ < 8; ++j_) dst[j_] = *(const bf16x8*)(ub_ + j_ * 1024 + voff); } while (0)
; #define LOADA(fd, ks_) do { _Pragma("unroll") for (int mi_ = 0; mi_ < 4; ++mi_) fd[mi_] = AFRAG(mi_, ks_); } while (0)
; DEVINL void phase4(const Params& P, unsigned char* smem) {
;     ...
;         if (!SKIPF(32)) {
;             const unsigned char* wb = (const unsigned char*)(P.ws + WS_WOF) + (size_t)(8 * wv) * 1024;
;             unsigned voff = (unsigned)(lane * 16);
;             asm volatile("" : "+v"(voff));
;             const int aoff = lr * 2048;
;     ...
;             bf16x8 b0[8], b1[8];
;     ...
;             bf16x8 fa[4];
;             LOADB(b0, 0); LOADA(fa, 0);
	s_cbranch_vccz .LBB0_587
	v_lshlrev_b32_e32 v178, 4, v190
	global_load_dwordx4 v[130:133], v178, s[44:45]
	global_load_dwordx4 v[134:137], v178, s[44:45] offset:1024
	global_load_dwordx4 v[138:141], v178, s[44:45] offset:2048
	global_load_dwordx4 v[142:145], v178, s[44:45] offset:3072
	v_lshl_add_u64 v[192:193], s[44:45], 0, v[178:179]
	v_add_co_u32_e32 v2, vcc, 0x1000, v192
	v_lshl_add_u32 v191, v238, 11, 0
	s_nop 0
	v_addc_co_u32_e32 v3, vcc, 0, v193, vcc
	global_load_dwordx4 v[158:161], v[2:3], off
	global_load_dwordx4 v[154:157], v[2:3], off offset:1024
	global_load_dwordx4 v[150:153], v[2:3], off offset:2048
	global_load_dwordx4 v[146:149], v[2:3], off offset:3072
	v_xor_b32_e32 v2, v204, v238
	v_lshl_add_u32 v2, v2, 4, v191
	v_add_u32_e32 v3, 0x10000, v2
	ds_read_b128 v[174:177], v2
	ds_read_b128 v[170:173], v2 offset:32768
	v_add_u32_e32 v2, 0x18000, v2
	ds_read_b128 v[166:169], v3
	ds_read_b128 v[162:165], v2
	v_mov_b32_e32 v34, 0
	s_mov_b32 s0, 0
	v_add_u32_e32 v196, 4, v204
	v_lshl_add_u64 v[194:195], s[52:53], 0, v[178:179]
	v_mov_b32_e32 v35, v34
	v_mov_b32_e32 v36, v34
	v_mov_b32_e32 v37, v34
	v_mov_b32_e32 v38, v34
	v_mov_b32_e32 v39, v34
	v_mov_b32_e32 v40, v34
	v_mov_b32_e32 v41, v34
	v_mov_b32_e32 v98, v34
	v_mov_b32_e32 v99, v34
	v_mov_b32_e32 v100, v34
	v_mov_b32_e32 v101, v34
	v_mov_b32_e32 v102, v34
	v_mov_b32_e32 v103, v34
	v_mov_b32_e32 v104, v34
	v_mov_b32_e32 v105, v34
	v_mov_b32_e32 v42, v34
	v_mov_b32_e32 v43, v34
	v_mov_b32_e32 v44, v34
	v_mov_b32_e32 v45, v34
	v_mov_b32_e32 v46, v34
	v_mov_b32_e32 v47, v34
	v_mov_b32_e32 v48, v34
	v_mov_b32_e32 v49, v34
	v_mov_b32_e32 v106, v34
	v_mov_b32_e32 v107, v34
	v_mov_b32_e32 v108, v34
	v_mov_b32_e32 v109, v34
	v_mov_b32_e32 v110, v34
	v_mov_b32_e32 v111, v34
	v_mov_b32_e32 v112, v34
	v_mov_b32_e32 v113, v34
	v_mov_b32_e32 v50, v34
	v_mov_b32_e32 v51, v34
	v_mov_b32_e32 v52, v34
	v_mov_b32_e32 v53, v34
	v_mov_b32_e32 v54, v34
	v_mov_b32_e32 v55, v34
	v_mov_b32_e32 v56, v34
	v_mov_b32_e32 v57, v34
	v_mov_b32_e32 v114, v34
	v_mov_b32_e32 v115, v34
	v_mov_b32_e32 v116, v34
	v_mov_b32_e32 v117, v34
	v_mov_b32_e32 v118, v34
	v_mov_b32_e32 v119, v34
	v_mov_b32_e32 v120, v34
	v_mov_b32_e32 v121, v34
	v_mov_b32_e32 v58, v34
	v_mov_b32_e32 v59, v34
	v_mov_b32_e32 v60, v34
	v_mov_b32_e32 v61, v34
	v_mov_b32_e32 v62, v34
	v_mov_b32_e32 v63, v34
	v_mov_b32_e32 v64, v34
	v_mov_b32_e32 v65, v34
	v_mov_b32_e32 v122, v34
	v_mov_b32_e32 v123, v34
	v_mov_b32_e32 v124, v34
	v_mov_b32_e32 v125, v34
	v_mov_b32_e32 v126, v34
	v_mov_b32_e32 v127, v34
	v_mov_b32_e32 v128, v34
	v_mov_b32_e32 v129, v34
	v_mov_b32_e32 v94, v34
	v_mov_b32_e32 v95, v34
	v_mov_b32_e32 v96, v34
	v_mov_b32_e32 v97, v34
	v_mov_b32_e32 v90, v34
	v_mov_b32_e32 v91, v34
	v_mov_b32_e32 v92, v34
	v_mov_b32_e32 v93, v34
	v_mov_b32_e32 v30, v34
	v_mov_b32_e32 v31, v34
	v_mov_b32_e32 v32, v34
	v_mov_b32_e32 v33, v34
	v_mov_b32_e32 v26, v34
	v_mov_b32_e32 v27, v34
	v_mov_b32_e32 v28, v34
	v_mov_b32_e32 v29, v34
	v_mov_b32_e32 v86, v34
	v_mov_b32_e32 v87, v34
	v_mov_b32_e32 v88, v34
	v_mov_b32_e32 v89, v34
	v_mov_b32_e32 v82, v34
	v_mov_b32_e32 v83, v34
	v_mov_b32_e32 v84, v34
	v_mov_b32_e32 v85, v34
	v_mov_b32_e32 v22, v34
	v_mov_b32_e32 v23, v34
	v_mov_b32_e32 v24, v34
	v_mov_b32_e32 v25, v34
	v_mov_b32_e32 v18, v34
	v_mov_b32_e32 v19, v34
	v_mov_b32_e32 v20, v34
	v_mov_b32_e32 v21, v34
	v_mov_b32_e32 v78, v34
	v_mov_b32_e32 v79, v34
	v_mov_b32_e32 v80, v34
	v_mov_b32_e32 v81, v34
	v_mov_b32_e32 v74, v34
	v_mov_b32_e32 v75, v34
	v_mov_b32_e32 v76, v34
	v_mov_b32_e32 v77, v34
	v_mov_b32_e32 v14, v34
	v_mov_b32_e32 v15, v34
	v_mov_b32_e32 v16, v34
	v_mov_b32_e32 v17, v34
	v_mov_b32_e32 v10, v34
	v_mov_b32_e32 v11, v34
	v_mov_b32_e32 v12, v34
	v_mov_b32_e32 v13, v34
	v_mov_b32_e32 v70, v34
	v_mov_b32_e32 v71, v34
	v_mov_b32_e32 v72, v34
	v_mov_b32_e32 v73, v34
	v_mov_b32_e32 v66, v34
	v_mov_b32_e32 v67, v34
	v_mov_b32_e32 v68, v34
	v_mov_b32_e32 v69, v34
	v_mov_b32_e32 v6, v34
	v_mov_b32_e32 v7, v34
	v_mov_b32_e32 v8, v34
	v_mov_b32_e32 v9, v34
	v_mov_b32_e32 v2, v34
	v_mov_b32_e32 v3, v34
	v_mov_b32_e32 v4, v34
	v_mov_b32_e32 v5, v34
